# speedup vs baseline: 1.0144x; 1.0012x over previous
.LBB0_8:
	s_or_b64 exec, exec, s[4:5]
	v_lshlrev_b32_e32 v3, 23, v3
	v_sub_u32_e32 v3, 0x7f000000, v3
	v_mul_f32_e32 v32, v161, v3
	v_lshrrev_b32_e32 v130, 2, v2
	v_lshrrev_b32_e32 v3, 7, v0
	v_lshl_add_u32 v130, v130, 1, v3
	v_lshlrev_b32_e32 v158, 10, v130
	v_and_b32_e32 v160, 3, v2
	v_sub_u32_e32 v160, v160, v3
	v_lshlrev_b32_e32 v160, 4, v160
	v_cndmask_b32_e64 v34, 0, 1, s[16:17]
	v_pk_mul_f32 v[2:3], v[32:33], v[126:127] op_sel_hi:[0,1]
	v_pk_mul_f32 v[4:5], v[32:33], v[128:129] op_sel_hi:[0,1]
	v_pk_mul_f32 v[18:19], v[32:33], v[118:119] op_sel_hi:[0,1]
	v_pk_mul_f32 v[20:21], v[32:33], v[120:121] op_sel_hi:[0,1]
	v_pk_mul_f32 v[6:7], v[32:33], v[122:123] op_sel_hi:[0,1]
	v_pk_mul_f32 v[8:9], v[32:33], v[124:125] op_sel_hi:[0,1]
	v_pk_mul_f32 v[22:23], v[32:33], v[106:107] op_sel_hi:[0,1]
	v_pk_mul_f32 v[24:25], v[32:33], v[108:109] op_sel_hi:[0,1]
	v_pk_mul_f32 v[10:11], v[32:33], v[114:115] op_sel_hi:[0,1]
	v_pk_mul_f32 v[12:13], v[32:33], v[116:117] op_sel_hi:[0,1]
	v_pk_mul_f32 v[26:27], v[32:33], v[102:103] op_sel_hi:[0,1]
	v_pk_mul_f32 v[28:29], v[32:33], v[104:105] op_sel_hi:[0,1]
	v_pk_mul_f32 v[14:15], v[32:33], v[110:111] op_sel_hi:[0,1]
	v_pk_mul_f32 v[16:17], v[32:33], v[112:113] op_sel_hi:[0,1]
	v_pk_mul_f32 v[30:31], v[32:33], v[98:99] op_sel_hi:[0,1]
	v_pk_mul_f32 v[32:33], v[32:33], v[100:101] op_sel_hi:[0,1]
	s_mov_b64 s[6:7], -1
	v_cmp_ne_u32_e64 s[4:5], 1, v34
	s_andn2_b64 vcc, exec, s[16:17]
	v_add_u32_e32 v34, v162, v160
	s_cbranch_vccz .LBB0_11
	s_load_dwordx2 s[12:13], s[0:1], 0x38
	s_andn2_b64 vcc, exec, s[6:7]
	v_mul_u32_u24_e32 v159, 0x600, v130
	s_cbranch_vccz .LBB0_12

.LBB0_100:
	s_mov_b64 s[4:5], -1
	s_and_b64 vcc, exec, s[16:17]
	s_waitcnt lgkmcnt(0)
	s_barrier
	s_cbranch_vccz .LBB0_104
	s_load_dwordx2 s[4:5], s[0:1], 0x18
	s_lshr_b32 s6, s3, 3
	s_mov_b32 s7, 0
	s_lshl_b64 s[6:7], s[6:7], 18
	s_and_b32 s8, s3, 7
	s_lshl_b32 s8, s8, 11
	v_lshrrev_b32_e32 v2, 7, v0
	v_lshlrev_b32_e32 v2, 14, v2
	v_and_b32_e32 v3, 0x7f, v0
	v_lshl_add_u32 v2, v3, 4, v2
	v_lshlrev_b32_e32 v1, 4, v0
	ds_read_b128 v[4:7], v1 offset:0
	ds_read_b128 v[8:11], v1 offset:4096
	ds_read_b128 v[12:15], v1 offset:8192
	ds_read_b128 v[16:19], v1 offset:12288
	ds_read_b128 v[20:23], v1 offset:16384
	ds_read_b128 v[24:27], v1 offset:20480
	ds_read_b128 v[28:31], v1 offset:24576
	ds_read_b128 v[32:35], v1 offset:28672
	s_waitcnt lgkmcnt(0)
	s_add_u32 s4, s4, s6
	s_addc_u32 s5, s5, s7
	s_add_u32 s4, s4, s8
	s_addc_u32 s5, s5, 0
	global_store_dwordx4 v2, v[4:7], s[4:5] nt
	v_add_u32_e32 v2, 0x8000, v2
	global_store_dwordx4 v2, v[8:11], s[4:5] nt
	v_add_u32_e32 v2, 0x8000, v2
	global_store_dwordx4 v2, v[12:15], s[4:5] nt
	v_add_u32_e32 v2, 0x8000, v2
	global_store_dwordx4 v2, v[16:19], s[4:5] nt
	v_add_u32_e32 v2, 0x8000, v2
	global_store_dwordx4 v2, v[20:23], s[4:5] nt
	v_add_u32_e32 v2, 0x8000, v2
	global_store_dwordx4 v2, v[24:27], s[4:5] nt
	v_add_u32_e32 v2, 0x8000, v2
	global_store_dwordx4 v2, v[28:31], s[4:5] nt
	v_add_u32_e32 v2, 0x8000, v2
	global_store_dwordx4 v2, v[32:35], s[4:5] nt
	s_branch .LBB0_107
.LBB0_104:
	s_and_b64 vcc, exec, s[4:5]
	s_cbranch_vccz .LBB0_107
	s_load_dwordx2 s[0:1], s[0:1], 0x20
	s_ashr_i32 s3, s2, 3
	s_mul_hi_i32 s4, s3, 0x60000
	s_mul_i32 s3, s3, 0x60000
	s_and_b32 s5, s2, 7
	s_mul_i32 s5, s5, 0xc00
	s_mov_b32 s6, 0xaaaaaaab
	s_waitcnt lgkmcnt(0)
	s_add_u32 s0, s0, s3
	s_addc_u32 s1, s1, s4
	s_add_u32 s0, s0, s5
	s_addc_u32 s1, s1, 0
	v_add_u32_e32 v4, 0x0, v0
	v_mul_hi_u32 v5, v4, s6
	v_lshrrev_b32_e32 v5, 7, v5
	v_mul_u32_u24_e32 v6, 0xc0, v5
	v_sub_u32_e32 v6, v4, v6
	v_mul_u32_u24_e32 v7, 0x6000, v5
	v_lshl_add_u32 v7, v6, 4, v7
	v_lshlrev_b32_e32 v4, 4, v4
	ds_read_b128 v[40:43], v4
	v_add_u32_e32 v12, 0x100, v0
	v_mul_hi_u32 v13, v12, s6
	v_lshrrev_b32_e32 v13, 7, v13
	v_mul_u32_u24_e32 v14, 0xc0, v13
	v_sub_u32_e32 v14, v12, v14
	v_mul_u32_u24_e32 v15, 0x6000, v13
	v_lshl_add_u32 v15, v14, 4, v15
	v_lshlrev_b32_e32 v12, 4, v12
	ds_read_b128 v[44:47], v12
	v_add_u32_e32 v20, 0x200, v0
	v_mul_hi_u32 v21, v20, s6
	v_lshrrev_b32_e32 v21, 7, v21
	v_mul_u32_u24_e32 v22, 0xc0, v21
	v_sub_u32_e32 v22, v20, v22
	v_mul_u32_u24_e32 v23, 0x6000, v21
	v_lshl_add_u32 v23, v22, 4, v23
	v_lshlrev_b32_e32 v20, 4, v20
	ds_read_b128 v[48:51], v20
	v_add_u32_e32 v28, 0x300, v0
	v_mul_hi_u32 v29, v28, s6
	v_lshrrev_b32_e32 v29, 7, v29
	v_mul_u32_u24_e32 v30, 0xc0, v29
	v_sub_u32_e32 v30, v28, v30
	v_mul_u32_u24_e32 v31, 0x6000, v29
	v_lshl_add_u32 v31, v30, 4, v31
	v_lshlrev_b32_e32 v28, 4, v28
	ds_read_b128 v[52:55], v28
	s_waitcnt lgkmcnt(0)
	global_store_dwordx4 v7, v[40:43], s[0:1] nt
	global_store_dwordx4 v15, v[44:47], s[0:1] nt
	global_store_dwordx4 v23, v[48:51], s[0:1] nt
	global_store_dwordx4 v31, v[52:55], s[0:1] nt
	s_nop 1
	v_add_u32_e32 v4, 0x400, v0
	v_mul_hi_u32 v5, v4, s6
	v_lshrrev_b32_e32 v5, 7, v5
	v_mul_u32_u24_e32 v6, 0xc0, v5
	v_sub_u32_e32 v6, v4, v6
	v_mul_u32_u24_e32 v7, 0x6000, v5
	v_lshl_add_u32 v7, v6, 4, v7
	v_lshlrev_b32_e32 v4, 4, v4
	ds_read_b128 v[40:43], v4
	v_add_u32_e32 v12, 0x500, v0
	v_mul_hi_u32 v13, v12, s6
	v_lshrrev_b32_e32 v13, 7, v13
	v_mul_u32_u24_e32 v14, 0xc0, v13
	v_sub_u32_e32 v14, v12, v14
	v_mul_u32_u24_e32 v15, 0x6000, v13
	v_lshl_add_u32 v15, v14, 4, v15
	v_lshlrev_b32_e32 v12, 4, v12
	ds_read_b128 v[44:47], v12
	v_add_u32_e32 v20, 0x600, v0
	v_mul_hi_u32 v21, v20, s6
	v_lshrrev_b32_e32 v21, 7, v21
	v_mul_u32_u24_e32 v22, 0xc0, v21
	v_sub_u32_e32 v22, v20, v22
	v_mul_u32_u24_e32 v23, 0x6000, v21
	v_lshl_add_u32 v23, v22, 4, v23
	v_lshlrev_b32_e32 v20, 4, v20
	ds_read_b128 v[48:51], v20
	v_add_u32_e32 v28, 0x700, v0
	v_mul_hi_u32 v29, v28, s6
	v_lshrrev_b32_e32 v29, 7, v29
	v_mul_u32_u24_e32 v30, 0xc0, v29
	v_sub_u32_e32 v30, v28, v30
	v_mul_u32_u24_e32 v31, 0x6000, v29
	v_lshl_add_u32 v31, v30, 4, v31
	v_lshlrev_b32_e32 v28, 4, v28
	ds_read_b128 v[52:55], v28
	s_waitcnt lgkmcnt(0)
	global_store_dwordx4 v7, v[40:43], s[0:1] nt
	global_store_dwordx4 v15, v[44:47], s[0:1] nt
	global_store_dwordx4 v23, v[48:51], s[0:1] nt
	global_store_dwordx4 v31, v[52:55], s[0:1] nt
	s_nop 1
	v_add_u32_e32 v4, 0x800, v0
	v_mul_hi_u32 v5, v4, s6
	v_lshrrev_b32_e32 v5, 7, v5
	v_mul_u32_u24_e32 v6, 0xc0, v5
	v_sub_u32_e32 v6, v4, v6
	v_mul_u32_u24_e32 v7, 0x6000, v5
	v_lshl_add_u32 v7, v6, 4, v7
	v_lshlrev_b32_e32 v4, 4, v4
	ds_read_b128 v[40:43], v4
	v_add_u32_e32 v12, 0x900, v0
	v_mul_hi_u32 v13, v12, s6
	v_lshrrev_b32_e32 v13, 7, v13
	v_mul_u32_u24_e32 v14, 0xc0, v13
	v_sub_u32_e32 v14, v12, v14
	v_mul_u32_u24_e32 v15, 0x6000, v13
	v_lshl_add_u32 v15, v14, 4, v15
	v_lshlrev_b32_e32 v12, 4, v12
	ds_read_b128 v[44:47], v12
	v_add_u32_e32 v20, 0xa00, v0
	v_mul_hi_u32 v21, v20, s6
	v_lshrrev_b32_e32 v21, 7, v21
	v_mul_u32_u24_e32 v22, 0xc0, v21
	v_sub_u32_e32 v22, v20, v22
	v_mul_u32_u24_e32 v23, 0x6000, v21
	v_lshl_add_u32 v23, v22, 4, v23
	v_lshlrev_b32_e32 v20, 4, v20
	ds_read_b128 v[48:51], v20
	v_add_u32_e32 v28, 0xb00, v0
	v_mul_hi_u32 v29, v28, s6
	v_lshrrev_b32_e32 v29, 7, v29
	v_mul_u32_u24_e32 v30, 0xc0, v29
	v_sub_u32_e32 v30, v28, v30
	v_mul_u32_u24_e32 v31, 0x6000, v29
	v_lshl_add_u32 v31, v30, 4, v31
	v_lshlrev_b32_e32 v28, 4, v28
	ds_read_b128 v[52:55], v28
	s_waitcnt lgkmcnt(0)
	global_store_dwordx4 v7, v[40:43], s[0:1] nt
	global_store_dwordx4 v15, v[44:47], s[0:1] nt
	global_store_dwordx4 v23, v[48:51], s[0:1] nt
	global_store_dwordx4 v31, v[52:55], s[0:1] nt
	s_nop 1

_Z15gemm_lse_kernelPKhS0_PKjS2_PfPiP15HIP_vector_typeIfLj2EE:
	s_load_dwordx4 s[64:67], s[0:1], 0x0
	s_load_dwordx4 s[8:11], s[0:1], 0x10
	s_load_dwordx4 s[12:15], s[0:1], 0x20
	s_load_dwordx2 s[16:17], s[0:1], 0x30
	v_and_b32_e32 v220, 63, v0
	v_lshlrev_b32_e32 v221, 4, v220
	v_add_u32_e32 v225, 0x2000, v221
	v_add_u32_e32 v226, 0x4000, v221
	v_mov_b32_e32 v251, 0
	v_readfirstlane_b32 s18, v0
	s_lshr_b32 s18, s18, 6
	s_lshr_b32 s19, s18, 2
	s_and_b32 s20, s18, 3
	s_lshl_b32 s48, s18, 10
	s_lshl_b32 s35, s19, 13
	v_add_u32_e32 v222, s35, v221
	s_mul_i32 s35, s20, 0x1800
	s_add_u32 s35, s35, 0x4000
	v_add_u32_e32 v223, s35, v221
	s_add_u32 s35, s35, 0x400
	v_lshl_add_u32 v224, v220, 3, s35
	s_mov_b32 s50, 0xffff0000
	s_mov_b32 s51, 0
	s_mov_b32 s52, 0
	s_mov_b32 s53, 0xffff
	s_mov_b32 s54, 0
	s_mov_b32 s55, 0xffff0000
	s_mov_b32 s56, 0xd800000
	s_mov_b32 s57, 0x71800000
	s_and_b32 s35, s2, 7
	s_lshr_b32 s36, s2, 3
	s_mul_i32 s21, s35, 0xfa
	s_add_u32 s21, s21, s36
	s_cmp_lt_u32 s36, 26
	s_cselect_b32 s22, 8, 7
	s_mov_b32 s23, 0
	s_lshr_b32 s80, s21, 5
	s_and_b32 s82, s21, 31
	s_lshr_b32 s83, s80, 1
	s_lshl_b32 s83, s83, 2
	s_lshr_b32 s84, s82, 3
	s_add_u32 s83, s83, s84
	s_and_b32 s84, s80, 1
	s_lshl_b32 s84, s84, 3
	s_and_b32 s85, s82, 7
	s_add_u32 s84, s84, s85
	s_sub_u32 s85, s21, 0x7c0
	s_cmpk_gt_u32 s21, 0x7bf
	s_cselect_b32 s24, 0x7c, s83
	s_cselect_b32 s25, s85, s84
	s_lshl_b32 s28, s24, 18
	s_mul_i32 s29, s25, 0x60000
	s_add_u32 s29, s29, 0x1f40000
	s_add_u32 s45, s23, 1
	s_sub_u32 s46, s22, 1
	s_min_u32 s45, s45, s46
	s_lshl_b32 s45, s45, 5
	s_add_u32 s45, s45, s21
	s_lshr_b32 s80, s45, 5
	s_and_b32 s82, s45, 31
	s_lshr_b32 s83, s80, 1
	s_lshl_b32 s83, s83, 2
	s_lshr_b32 s84, s82, 3
	s_add_u32 s83, s83, s84
	s_and_b32 s84, s80, 1
	s_lshl_b32 s84, s84, 3
	s_and_b32 s85, s82, 7
	s_add_u32 s84, s84, s85
	s_sub_u32 s85, s45, 0x7c0
	s_cmpk_gt_u32 s45, 0x7bf
	s_cselect_b32 s26, 0x7c, s83
	s_cselect_b32 s27, s85, s84
	s_lshl_b32 s30, s26, 18
	s_mul_i32 s31, s27, 0x60000
	s_add_u32 s31, s31, 0x1f40000
	s_add_u32 s38, s30, s48
	s_add_u32 s39, s31, s48
	s_waitcnt lgkmcnt(0)
	s_mov_b32 s4, s64
	s_and_b32 s5, s65, 0xffff
	s_mov_b32 s6, 0x2540000
	s_mov_b32 s7, 0x20000
	s_mov_b32 s44, 0
	s_cmp_lt_u32 s18, 4
	s_cselect_b32 s80, s24, s25
	s_cselect_b32 s82, s8, s10
	s_cselect_b32 s83, s9, s11
	s_lshl_b32 s80, s80, 10
	s_and_b32 s84, s18, 3
	s_lshl_b32 s84, s84, 8
	s_add_u32 s80, s80, s84
	s_add_u32 s82, s82, s80
	s_addc_u32 s83, s83, 0
	s_lshl_b32 s84, s44, 11
	s_lshl_b32 s85, s18, 8
	s_add_u32 s84, s84, s85
	s_add_u32 s84, s84, 0x1e000
	s_mov_b32 m0, s84
	v_lshlrev_b32_e32 v236, 2, v220
	global_load_lds_dword v236, s[82:83]
	s_add_u32 s36, s28, s48
	s_add_u32 s37, s29, s48
	s_mov_b32 s40, s48
	s_add_u32 s49, s48, 0x1e000
	s_mov_b32 s34, 0
	s_mov_b32 m0, s40
	s_nop 0
	buffer_load_dwordx4 v221, s[4:7], s36 offen lds
	s_add_u32 m0, s40, 0x2000
	s_nop 0
	buffer_load_dwordx4 v225, s[4:7], s36 offen lds
	s_add_u32 m0, s40, 0x4000
	s_nop 0
	buffer_load_dwordx4 v221, s[4:7], s37 offen lds
	s_add_u32 m0, s40, 0x6000
	s_nop 0
	buffer_load_dwordx4 v225, s[4:7], s37 offen lds
	s_add_u32 m0, s40, 0x8000
	s_nop 0
	buffer_load_dwordx4 v226, s[4:7], s37 offen lds
	s_add_u32 s36, s36, 0x4000
	s_add_u32 s37, s37, 0x6000
	s_add_u32 s40, s40, 0xa000
	s_sub_u32 s41, s40, 0x1e000
	s_cmp_ge_u32 s40, s49
	s_cselect_b32 s40, s41, s40
	s_mov_b32 m0, s40
	s_nop 0
	buffer_load_dwordx4 v221, s[4:7], s36 offen lds
	s_add_u32 m0, s40, 0x2000
	s_nop 0
	buffer_load_dwordx4 v225, s[4:7], s36 offen lds
	s_add_u32 m0, s40, 0x4000
	s_nop 0
	buffer_load_dwordx4 v221, s[4:7], s37 offen lds
	s_add_u32 m0, s40, 0x6000
	s_nop 0
	buffer_load_dwordx4 v225, s[4:7], s37 offen lds
	s_add_u32 m0, s40, 0x8000
	s_nop 0
	buffer_load_dwordx4 v226, s[4:7], s37 offen lds
	s_add_u32 s36, s36, 0x4000
	s_add_u32 s37, s37, 0x6000
	s_add_u32 s40, s40, 0xa000
	s_sub_u32 s41, s40, 0x1e000
	s_cmp_ge_u32 s40, s49
	s_cselect_b32 s40, s41, s40
	s_mov_b32 m0, s40
	s_nop 0
	buffer_load_dwordx4 v221, s[4:7], s36 offen lds
	s_add_u32 m0, s40, 0x2000
	s_nop 0
	buffer_load_dwordx4 v225, s[4:7], s36 offen lds
	s_add_u32 m0, s40, 0x4000
	s_nop 0
	buffer_load_dwordx4 v221, s[4:7], s37 offen lds
	s_add_u32 m0, s40, 0x6000
	s_nop 0
	buffer_load_dwordx4 v225, s[4:7], s37 offen lds
	s_add_u32 m0, s40, 0x8000
	s_nop 0
	buffer_load_dwordx4 v226, s[4:7], s37 offen lds
	s_add_u32 s36, s36, 0x4000
	s_add_u32 s37, s37, 0x6000
	s_add_u32 s40, s40, 0xa000
	s_sub_u32 s41, s40, 0x1e000
	s_cmp_ge_u32 s40, s49
	s_cselect_b32 s40, s41, s40
	s_mov_b32 s33, 0
	s_waitcnt vmcnt(10)
	s_barrier
	s_mov_b32 s44, 0
	s_lshl_b32 s80, s44, 11
	s_add_u32 s80, s80, 0x1e000
	s_lshl_b32 s82, s19, 9
	s_add_u32 s82, s82, s80
	s_lshl_b32 s83, s20, 8
	s_add_u32 s83, s83, s80
	s_add_u32 s83, s83, 0x400
	v_and_b32_e32 v234, 15, v220
	v_lshlrev_b32_e32 v234, 2, v234
	v_add_u32_e32 v235, s83, v234
	v_add_u32_e32 v234, s82, v234
	ds_read_b32 v208, v234 offset:0
	ds_read_b32 v209, v234 offset:64
	ds_read_b32 v210, v234 offset:128
	ds_read_b32 v211, v234 offset:192
	ds_read_b32 v212, v234 offset:256
	ds_read_b32 v213, v234 offset:320
	ds_read_b32 v214, v234 offset:384
	ds_read_b32 v215, v234 offset:448
	ds_read_b32 v216, v235 offset:0
	ds_read_b32 v217, v235 offset:64
	ds_read_b32 v218, v235 offset:128
	ds_read_b32 v219, v235 offset:192
	s_mul_i32 s35, s33, 0xa000
	v_add_u32_e32 v240, s35, v222
	v_add_u32_e32 v241, s35, v223
	v_add_u32_e32 v242, s35, v224
	s_add_u32 s33, s33, 1
	s_cmp_eq_u32 s33, 3
	s_cselect_b32 s33, 0, s33
	ds_read_b128 v[160:163], v241 offset:0
	ds_read_b64 v[164:165], v242 offset:0
	ds_read_b128 v[166:169], v241 offset:1536
	ds_read_b64 v[170:171], v242 offset:1536
	ds_read_b128 v[172:175], v241 offset:3072
	ds_read_b64 v[176:177], v242 offset:3072
	ds_read_b128 v[178:181], v241 offset:4608
	ds_read_b64 v[182:183], v242 offset:4608
	ds_read_b128 v[128:131], v240 offset:0
	ds_read_b128 v[132:135], v240 offset:1024
	ds_read_b128 v[136:139], v240 offset:2048
	ds_read_b128 v[140:143], v240 offset:3072
	ds_read_b128 v[144:147], v240 offset:4096
	ds_read_b128 v[148:151], v240 offset:5120
	ds_read_b128 v[152:155], v240 offset:6144
	ds_read_b128 v[156:159], v240 offset:7168
	s_lshl_b32 s80, s25, 8
	s_lshl_b32 s82, s20, 6
	s_add_u32 s80, s80, s82
	v_add_u32_e32 v250, s80, v220
	v_lshl_add_u64 v[248:249], v[250:251], 2, s[12:13]
	s_cmp_ge_u32 s18, 4
	s_cbranch_scc1 .Ltile1
.Ltile0:
	s_mov_b32 s34, 0
	s_waitcnt vmcnt(5)
	s_waitcnt lgkmcnt(0)
	s_barrier
	s_mul_i32 s35, s33, 0xa000
	v_add_u32_e32 v240, s35, v222
	v_add_u32_e32 v241, s35, v223
	v_add_u32_e32 v242, s35, v224
	s_add_u32 s33, s33, 1
	s_cmp_eq_u32 s33, 3
	s_cselect_b32 s33, 0, s33
	ds_read_b128 v[244:247], v240 offset:6144
	ds_read_b128 v[252:255], v240 offset:7168
	v_mfma_scale_f32_16x16x128_f8f6f4 v[0:3], v[128:131], v[160:165], 0, v208, v216 op_sel_hi:[0,0,0] cbsz:4 blgp:2
	v_mfma_scale_f32_16x16x128_f8f6f4 v[4:7], v[128:131], v[166:171], 0, v208, v217 op_sel_hi:[0,0,0] cbsz:4 blgp:2
	v_mfma_scale_f32_16x16x128_f8f6f4 v[8:11], v[128:131], v[172:177], 0, v208, v218 op_sel_hi:[0,0,0] cbsz:4 blgp:2
	v_mfma_scale_f32_16x16x128_f8f6f4 v[12:15], v[128:131], v[178:183], 0, v208, v219 op_sel_hi:[0,0,0] cbsz:4 blgp:2
	ds_read_b128 v[128:131], v240 offset:0
	ds_read_b128 v[184:187], v241 offset:0
	ds_read_b64 v[188:189], v242 offset:0
	v_mfma_scale_f32_16x16x128_f8f6f4 v[16:19], v[132:135], v[160:165], 0, v209, v216 op_sel_hi:[0,0,0] cbsz:4 blgp:2
	v_mfma_scale_f32_16x16x128_f8f6f4 v[20:23], v[132:135], v[166:171], 0, v209, v217 op_sel_hi:[0,0,0] cbsz:4 blgp:2
	v_mfma_scale_f32_16x16x128_f8f6f4 v[24:27], v[132:135], v[172:177], 0, v209, v218 op_sel_hi:[0,0,0] cbsz:4 blgp:2
	v_mfma_scale_f32_16x16x128_f8f6f4 v[28:31], v[132:135], v[178:183], 0, v209, v219 op_sel_hi:[0,0,0] cbsz:4 blgp:2
	s_cmp_eq_u32 s34, 13
	s_cselect_b32 s36, s38, s36
	s_cselect_b32 s37, s39, s37
	s_mov_b32 m0, s40
	ds_read_b128 v[132:135], v240 offset:1024
	ds_read_b128 v[190:193], v241 offset:1536
	ds_read_b64 v[194:195], v242 offset:1536
	buffer_load_dwordx4 v221, s[4:7], s36 offen lds
	v_mfma_scale_f32_16x16x128_f8f6f4 v[32:35], v[136:139], v[160:165], 0, v210, v216 op_sel_hi:[0,0,0] cbsz:4 blgp:2
	v_mfma_scale_f32_16x16x128_f8f6f4 v[36:39], v[136:139], v[166:171], 0, v210, v217 op_sel_hi:[0,0,0] cbsz:4 blgp:2
	v_mfma_scale_f32_16x16x128_f8f6f4 v[40:43], v[136:139], v[172:177], 0, v210, v218 op_sel_hi:[0,0,0] cbsz:4 blgp:2
	v_mfma_scale_f32_16x16x128_f8f6f4 v[44:47], v[136:139], v[178:183], 0, v210, v219 op_sel_hi:[0,0,0] cbsz:4 blgp:2
	s_add_u32 m0, s40, 0x2000
	ds_read_b128 v[136:139], v240 offset:2048
	ds_read_b128 v[196:199], v241 offset:3072
	ds_read_b64 v[200:201], v242 offset:3072
	buffer_load_dwordx4 v225, s[4:7], s36 offen lds
	v_mfma_scale_f32_16x16x128_f8f6f4 v[48:51], v[140:143], v[160:165], 0, v211, v216 op_sel_hi:[0,0,0] cbsz:4 blgp:2
	v_mfma_scale_f32_16x16x128_f8f6f4 v[52:55], v[140:143], v[166:171], 0, v211, v217 op_sel_hi:[0,0,0] cbsz:4 blgp:2
	v_mfma_scale_f32_16x16x128_f8f6f4 v[56:59], v[140:143], v[172:177], 0, v211, v218 op_sel_hi:[0,0,0] cbsz:4 blgp:2
	v_mfma_scale_f32_16x16x128_f8f6f4 v[60:63], v[140:143], v[178:183], 0, v211, v219 op_sel_hi:[0,0,0] cbsz:4 blgp:2
	s_add_u32 m0, s40, 0x4000
	ds_read_b128 v[140:143], v240 offset:3072
	ds_read_b128 v[202:205], v241 offset:4608
	ds_read_b64 v[206:207], v242 offset:4608
	buffer_load_dwordx4 v221, s[4:7], s37 offen lds
	v_mfma_scale_f32_16x16x128_f8f6f4 v[64:67], v[144:147], v[160:165], 0, v212, v216 op_sel_hi:[0,0,0] cbsz:4 blgp:2
	v_mfma_scale_f32_16x16x128_f8f6f4 v[68:71], v[144:147], v[166:171], 0, v212, v217 op_sel_hi:[0,0,0] cbsz:4 blgp:2
	v_mfma_scale_f32_16x16x128_f8f6f4 v[72:75], v[144:147], v[172:177], 0, v212, v218 op_sel_hi:[0,0,0] cbsz:4 blgp:2
	v_mfma_scale_f32_16x16x128_f8f6f4 v[76:79], v[144:147], v[178:183], 0, v212, v219 op_sel_hi:[0,0,0] cbsz:4 blgp:2
	s_add_u32 m0, s40, 0x6000
	ds_read_b128 v[144:147], v240 offset:4096
	buffer_load_dwordx4 v225, s[4:7], s37 offen lds
	v_mfma_scale_f32_16x16x128_f8f6f4 v[80:83], v[148:151], v[160:165], 0, v213, v216 op_sel_hi:[0,0,0] cbsz:4 blgp:2
	v_mfma_scale_f32_16x16x128_f8f6f4 v[84:87], v[148:151], v[166:171], 0, v213, v217 op_sel_hi:[0,0,0] cbsz:4 blgp:2
	v_mfma_scale_f32_16x16x128_f8f6f4 v[88:91], v[148:151], v[172:177], 0, v213, v218 op_sel_hi:[0,0,0] cbsz:4 blgp:2
	v_mfma_scale_f32_16x16x128_f8f6f4 v[92:95], v[148:151], v[178:183], 0, v213, v219 op_sel_hi:[0,0,0] cbsz:4 blgp:2
	s_add_u32 m0, s40, 0x8000
	ds_read_b128 v[148:151], v240 offset:5120
	buffer_load_dwordx4 v226, s[4:7], s37 offen lds
	s_add_u32 s36, s36, 0x4000
	s_add_u32 s37, s37, 0x6000
	s_add_u32 s40, s40, 0xa000
	s_sub_u32 s41, s40, 0x1e000
	s_cmp_ge_u32 s40, s49
	s_cselect_b32 s40, s41, s40
	v_mfma_scale_f32_16x16x128_f8f6f4 v[96:99], v[152:155], v[160:165], 0, v214, v216 op_sel_hi:[0,0,0] cbsz:4 blgp:2
	v_mfma_scale_f32_16x16x128_f8f6f4 v[100:103], v[152:155], v[166:171], 0, v214, v217 op_sel_hi:[0,0,0] cbsz:4 blgp:2
	v_mfma_scale_f32_16x16x128_f8f6f4 v[104:107], v[152:155], v[172:177], 0, v214, v218 op_sel_hi:[0,0,0] cbsz:4 blgp:2
	v_mfma_scale_f32_16x16x128_f8f6f4 v[108:111], v[152:155], v[178:183], 0, v214, v219 op_sel_hi:[0,0,0] cbsz:4 blgp:2
	v_mfma_scale_f32_16x16x128_f8f6f4 v[112:115], v[156:159], v[160:165], 0, v215, v216 op_sel_hi:[0,0,0] cbsz:4 blgp:2
	v_mfma_scale_f32_16x16x128_f8f6f4 v[116:119], v[156:159], v[166:171], 0, v215, v217 op_sel_hi:[0,0,0] cbsz:4 blgp:2
	v_mfma_scale_f32_16x16x128_f8f6f4 v[120:123], v[156:159], v[172:177], 0, v215, v218 op_sel_hi:[0,0,0] cbsz:4 blgp:2
	v_mfma_scale_f32_16x16x128_f8f6f4 v[124:127], v[156:159], v[178:183], 0, v215, v219 op_sel_hi:[0,0,0] cbsz:4 blgp:2
	s_add_u32 s34, s34, 1
	s_waitcnt vmcnt(5)
	s_waitcnt lgkmcnt(0)
	s_barrier
	s_mul_i32 s35, s33, 0xa000
	v_add_u32_e32 v240, s35, v222
	v_add_u32_e32 v241, s35, v223
	v_add_u32_e32 v242, s35, v224
	s_add_u32 s33, s33, 1
	s_cmp_eq_u32 s33, 3
	s_cselect_b32 s33, 0, s33
	ds_read_b128 v[152:155], v240 offset:6144
	ds_read_b128 v[156:159], v240 offset:7168
	v_mfma_scale_f32_16x16x128_f8f6f4 v[0:3], v[128:131], v[184:189], v[0:3], v208, v216 op_sel_hi:[0,0,0] cbsz:4 blgp:2
	v_mfma_scale_f32_16x16x128_f8f6f4 v[4:7], v[128:131], v[190:195], v[4:7], v208, v217 op_sel_hi:[0,0,0] cbsz:4 blgp:2
	v_mfma_scale_f32_16x16x128_f8f6f4 v[8:11], v[128:131], v[196:201], v[8:11], v208, v218 op_sel_hi:[0,0,0] cbsz:4 blgp:2
	v_mfma_scale_f32_16x16x128_f8f6f4 v[12:15], v[128:131], v[202:207], v[12:15], v208, v219 op_sel_hi:[0,0,0] cbsz:4 blgp:2
	ds_read_b128 v[128:131], v240 offset:0
	ds_read_b128 v[160:163], v241 offset:0
	ds_read_b64 v[164:165], v242 offset:0
	v_mfma_scale_f32_16x16x128_f8f6f4 v[16:19], v[132:135], v[184:189], v[16:19], v209, v216 op_sel_hi:[0,0,0] cbsz:4 blgp:2
	v_mfma_scale_f32_16x16x128_f8f6f4 v[20:23], v[132:135], v[190:195], v[20:23], v209, v217 op_sel_hi:[0,0,0] cbsz:4 blgp:2
	v_mfma_scale_f32_16x16x128_f8f6f4 v[24:27], v[132:135], v[196:201], v[24:27], v209, v218 op_sel_hi:[0,0,0] cbsz:4 blgp:2
	v_mfma_scale_f32_16x16x128_f8f6f4 v[28:31], v[132:135], v[202:207], v[28:31], v209, v219 op_sel_hi:[0,0,0] cbsz:4 blgp:2
	s_cmp_eq_u32 s34, 13
	s_cselect_b32 s36, s38, s36
	s_cselect_b32 s37, s39, s37
	s_mov_b32 m0, s40
	ds_read_b128 v[132:135], v240 offset:1024
	ds_read_b128 v[166:169], v241 offset:1536
	ds_read_b64 v[170:171], v242 offset:1536
	buffer_load_dwordx4 v221, s[4:7], s36 offen lds
	v_mfma_scale_f32_16x16x128_f8f6f4 v[32:35], v[136:139], v[184:189], v[32:35], v210, v216 op_sel_hi:[0,0,0] cbsz:4 blgp:2
	v_mfma_scale_f32_16x16x128_f8f6f4 v[36:39], v[136:139], v[190:195], v[36:39], v210, v217 op_sel_hi:[0,0,0] cbsz:4 blgp:2
	v_mfma_scale_f32_16x16x128_f8f6f4 v[40:43], v[136:139], v[196:201], v[40:43], v210, v218 op_sel_hi:[0,0,0] cbsz:4 blgp:2
	v_mfma_scale_f32_16x16x128_f8f6f4 v[44:47], v[136:139], v[202:207], v[44:47], v210, v219 op_sel_hi:[0,0,0] cbsz:4 blgp:2
	s_add_u32 m0, s40, 0x2000
	ds_read_b128 v[136:139], v240 offset:2048
	ds_read_b128 v[172:175], v241 offset:3072
	ds_read_b64 v[176:177], v242 offset:3072
	buffer_load_dwordx4 v225, s[4:7], s36 offen lds
	v_mfma_scale_f32_16x16x128_f8f6f4 v[48:51], v[140:143], v[184:189], v[48:51], v211, v216 op_sel_hi:[0,0,0] cbsz:4 blgp:2
	v_mfma_scale_f32_16x16x128_f8f6f4 v[52:55], v[140:143], v[190:195], v[52:55], v211, v217 op_sel_hi:[0,0,0] cbsz:4 blgp:2
	v_mfma_scale_f32_16x16x128_f8f6f4 v[56:59], v[140:143], v[196:201], v[56:59], v211, v218 op_sel_hi:[0,0,0] cbsz:4 blgp:2
	v_mfma_scale_f32_16x16x128_f8f6f4 v[60:63], v[140:143], v[202:207], v[60:63], v211, v219 op_sel_hi:[0,0,0] cbsz:4 blgp:2
	s_add_u32 m0, s40, 0x4000
	ds_read_b128 v[140:143], v240 offset:3072
	ds_read_b128 v[178:181], v241 offset:4608
	ds_read_b64 v[182:183], v242 offset:4608
	buffer_load_dwordx4 v221, s[4:7], s37 offen lds
	v_mfma_scale_f32_16x16x128_f8f6f4 v[64:67], v[144:147], v[184:189], v[64:67], v212, v216 op_sel_hi:[0,0,0] cbsz:4 blgp:2
	v_mfma_scale_f32_16x16x128_f8f6f4 v[68:71], v[144:147], v[190:195], v[68:71], v212, v217 op_sel_hi:[0,0,0] cbsz:4 blgp:2
	v_mfma_scale_f32_16x16x128_f8f6f4 v[72:75], v[144:147], v[196:201], v[72:75], v212, v218 op_sel_hi:[0,0,0] cbsz:4 blgp:2
	v_mfma_scale_f32_16x16x128_f8f6f4 v[76:79], v[144:147], v[202:207], v[76:79], v212, v219 op_sel_hi:[0,0,0] cbsz:4 blgp:2
	s_add_u32 m0, s40, 0x6000
	ds_read_b128 v[144:147], v240 offset:4096
	buffer_load_dwordx4 v225, s[4:7], s37 offen lds
	v_mfma_scale_f32_16x16x128_f8f6f4 v[80:83], v[148:151], v[184:189], v[80:83], v213, v216 op_sel_hi:[0,0,0] cbsz:4 blgp:2
	v_mfma_scale_f32_16x16x128_f8f6f4 v[84:87], v[148:151], v[190:195], v[84:87], v213, v217 op_sel_hi:[0,0,0] cbsz:4 blgp:2
	v_mfma_scale_f32_16x16x128_f8f6f4 v[88:91], v[148:151], v[196:201], v[88:91], v213, v218 op_sel_hi:[0,0,0] cbsz:4 blgp:2
	v_mfma_scale_f32_16x16x128_f8f6f4 v[92:95], v[148:151], v[202:207], v[92:95], v213, v219 op_sel_hi:[0,0,0] cbsz:4 blgp:2
	s_add_u32 m0, s40, 0x8000
	ds_read_b128 v[148:151], v240 offset:5120
	buffer_load_dwordx4 v226, s[4:7], s37 offen lds
	s_add_u32 s36, s36, 0x4000
	s_add_u32 s37, s37, 0x6000
	s_add_u32 s40, s40, 0xa000
	s_sub_u32 s41, s40, 0x1e000
	s_cmp_ge_u32 s40, s49
	s_cselect_b32 s40, s41, s40
	v_mfma_scale_f32_16x16x128_f8f6f4 v[96:99], v[244:247], v[184:189], v[96:99], v214, v216 op_sel_hi:[0,0,0] cbsz:4 blgp:2
	v_mfma_scale_f32_16x16x128_f8f6f4 v[100:103], v[244:247], v[190:195], v[100:103], v214, v217 op_sel_hi:[0,0,0] cbsz:4 blgp:2
	v_mfma_scale_f32_16x16x128_f8f6f4 v[104:107], v[244:247], v[196:201], v[104:107], v214, v218 op_sel_hi:[0,0,0] cbsz:4 blgp:2
	v_mfma_scale_f32_16x16x128_f8f6f4 v[108:111], v[244:247], v[202:207], v[108:111], v214, v219 op_sel_hi:[0,0,0] cbsz:4 blgp:2
	v_mfma_scale_f32_16x16x128_f8f6f4 v[112:115], v[252:255], v[184:189], v[112:115], v215, v216 op_sel_hi:[0,0,0] cbsz:4 blgp:2
	v_mfma_scale_f32_16x16x128_f8f6f4 v[116:119], v[252:255], v[190:195], v[116:119], v215, v217 op_sel_hi:[0,0,0] cbsz:4 blgp:2
	v_mfma_scale_f32_16x16x128_f8f6f4 v[120:123], v[252:255], v[196:201], v[120:123], v215, v218 op_sel_hi:[0,0,0] cbsz:4 blgp:2
	v_mfma_scale_f32_16x16x128_f8f6f4 v[124:127], v[252:255], v[202:207], v[124:127], v215, v219 op_sel_hi:[0,0,0] cbsz:4 blgp:2
	s_add_u32 s34, s34, 1
.Lkloop0:
	s_waitcnt vmcnt(5)
	s_waitcnt lgkmcnt(0)
	s_barrier
	s_mul_i32 s35, s33, 0xa000
	v_add_u32_e32 v240, s35, v222
	v_add_u32_e32 v241, s35, v223
	v_add_u32_e32 v242, s35, v224
	s_add_u32 s33, s33, 1
	s_cmp_eq_u32 s33, 3
	s_cselect_b32 s33, 0, s33
	ds_read_b128 v[244:247], v240 offset:6144
	ds_read_b128 v[252:255], v240 offset:7168
	v_mfma_scale_f32_16x16x128_f8f6f4 v[0:3], v[128:131], v[160:165], v[0:3], v208, v216 op_sel_hi:[0,0,0] cbsz:4 blgp:2
	v_mfma_scale_f32_16x16x128_f8f6f4 v[4:7], v[128:131], v[166:171], v[4:7], v208, v217 op_sel_hi:[0,0,0] cbsz:4 blgp:2
	v_mfma_scale_f32_16x16x128_f8f6f4 v[8:11], v[128:131], v[172:177], v[8:11], v208, v218 op_sel_hi:[0,0,0] cbsz:4 blgp:2
	v_mfma_scale_f32_16x16x128_f8f6f4 v[12:15], v[128:131], v[178:183], v[12:15], v208, v219 op_sel_hi:[0,0,0] cbsz:4 blgp:2
	ds_read_b128 v[128:131], v240 offset:0
	ds_read_b128 v[184:187], v241 offset:0
	ds_read_b64 v[188:189], v242 offset:0
	v_mfma_scale_f32_16x16x128_f8f6f4 v[16:19], v[132:135], v[160:165], v[16:19], v209, v216 op_sel_hi:[0,0,0] cbsz:4 blgp:2
	v_mfma_scale_f32_16x16x128_f8f6f4 v[20:23], v[132:135], v[166:171], v[20:23], v209, v217 op_sel_hi:[0,0,0] cbsz:4 blgp:2
	v_mfma_scale_f32_16x16x128_f8f6f4 v[24:27], v[132:135], v[172:177], v[24:27], v209, v218 op_sel_hi:[0,0,0] cbsz:4 blgp:2
	v_mfma_scale_f32_16x16x128_f8f6f4 v[28:31], v[132:135], v[178:183], v[28:31], v209, v219 op_sel_hi:[0,0,0] cbsz:4 blgp:2
	s_cmp_eq_u32 s34, 13
	s_cselect_b32 s36, s38, s36
	s_cselect_b32 s37, s39, s37
	s_mov_b32 m0, s40
	ds_read_b128 v[132:135], v240 offset:1024
	ds_read_b128 v[190:193], v241 offset:1536
	ds_read_b64 v[194:195], v242 offset:1536
	buffer_load_dwordx4 v221, s[4:7], s36 offen lds
	v_mfma_scale_f32_16x16x128_f8f6f4 v[32:35], v[136:139], v[160:165], v[32:35], v210, v216 op_sel_hi:[0,0,0] cbsz:4 blgp:2
	v_mfma_scale_f32_16x16x128_f8f6f4 v[36:39], v[136:139], v[166:171], v[36:39], v210, v217 op_sel_hi:[0,0,0] cbsz:4 blgp:2
	v_mfma_scale_f32_16x16x128_f8f6f4 v[40:43], v[136:139], v[172:177], v[40:43], v210, v218 op_sel_hi:[0,0,0] cbsz:4 blgp:2
	v_mfma_scale_f32_16x16x128_f8f6f4 v[44:47], v[136:139], v[178:183], v[44:47], v210, v219 op_sel_hi:[0,0,0] cbsz:4 blgp:2
	s_add_u32 m0, s40, 0x2000
	ds_read_b128 v[136:139], v240 offset:2048
	ds_read_b128 v[196:199], v241 offset:3072
	ds_read_b64 v[200:201], v242 offset:3072
	buffer_load_dwordx4 v225, s[4:7], s36 offen lds
	v_mfma_scale_f32_16x16x128_f8f6f4 v[48:51], v[140:143], v[160:165], v[48:51], v211, v216 op_sel_hi:[0,0,0] cbsz:4 blgp:2
	v_mfma_scale_f32_16x16x128_f8f6f4 v[52:55], v[140:143], v[166:171], v[52:55], v211, v217 op_sel_hi:[0,0,0] cbsz:4 blgp:2
	v_mfma_scale_f32_16x16x128_f8f6f4 v[56:59], v[140:143], v[172:177], v[56:59], v211, v218 op_sel_hi:[0,0,0] cbsz:4 blgp:2
	v_mfma_scale_f32_16x16x128_f8f6f4 v[60:63], v[140:143], v[178:183], v[60:63], v211, v219 op_sel_hi:[0,0,0] cbsz:4 blgp:2
	s_add_u32 m0, s40, 0x4000
	ds_read_b128 v[140:143], v240 offset:3072
	ds_read_b128 v[202:205], v241 offset:4608
	ds_read_b64 v[206:207], v242 offset:4608
	buffer_load_dwordx4 v221, s[4:7], s37 offen lds
	v_mfma_scale_f32_16x16x128_f8f6f4 v[64:67], v[144:147], v[160:165], v[64:67], v212, v216 op_sel_hi:[0,0,0] cbsz:4 blgp:2
	v_mfma_scale_f32_16x16x128_f8f6f4 v[68:71], v[144:147], v[166:171], v[68:71], v212, v217 op_sel_hi:[0,0,0] cbsz:4 blgp:2
	v_mfma_scale_f32_16x16x128_f8f6f4 v[72:75], v[144:147], v[172:177], v[72:75], v212, v218 op_sel_hi:[0,0,0] cbsz:4 blgp:2
	v_mfma_scale_f32_16x16x128_f8f6f4 v[76:79], v[144:147], v[178:183], v[76:79], v212, v219 op_sel_hi:[0,0,0] cbsz:4 blgp:2
	s_add_u32 m0, s40, 0x6000
	ds_read_b128 v[144:147], v240 offset:4096
	buffer_load_dwordx4 v225, s[4:7], s37 offen lds
	v_mfma_scale_f32_16x16x128_f8f6f4 v[80:83], v[148:151], v[160:165], v[80:83], v213, v216 op_sel_hi:[0,0,0] cbsz:4 blgp:2
	v_mfma_scale_f32_16x16x128_f8f6f4 v[84:87], v[148:151], v[166:171], v[84:87], v213, v217 op_sel_hi:[0,0,0] cbsz:4 blgp:2
	v_mfma_scale_f32_16x16x128_f8f6f4 v[88:91], v[148:151], v[172:177], v[88:91], v213, v218 op_sel_hi:[0,0,0] cbsz:4 blgp:2
	v_mfma_scale_f32_16x16x128_f8f6f4 v[92:95], v[148:151], v[178:183], v[92:95], v213, v219 op_sel_hi:[0,0,0] cbsz:4 blgp:2
	s_add_u32 m0, s40, 0x8000
	ds_read_b128 v[148:151], v240 offset:5120
	buffer_load_dwordx4 v226, s[4:7], s37 offen lds
	s_add_u32 s36, s36, 0x4000
	s_add_u32 s37, s37, 0x6000
	s_add_u32 s40, s40, 0xa000
	s_sub_u32 s41, s40, 0x1e000
	s_cmp_ge_u32 s40, s49
	s_cselect_b32 s40, s41, s40
	v_mfma_scale_f32_16x16x128_f8f6f4 v[96:99], v[152:155], v[160:165], v[96:99], v214, v216 op_sel_hi:[0,0,0] cbsz:4 blgp:2
	v_mfma_scale_f32_16x16x128_f8f6f4 v[100:103], v[152:155], v[166:171], v[100:103], v214, v217 op_sel_hi:[0,0,0] cbsz:4 blgp:2
	v_mfma_scale_f32_16x16x128_f8f6f4 v[104:107], v[152:155], v[172:177], v[104:107], v214, v218 op_sel_hi:[0,0,0] cbsz:4 blgp:2
	v_mfma_scale_f32_16x16x128_f8f6f4 v[108:111], v[152:155], v[178:183], v[108:111], v214, v219 op_sel_hi:[0,0,0] cbsz:4 blgp:2
	v_mfma_scale_f32_16x16x128_f8f6f4 v[112:115], v[156:159], v[160:165], v[112:115], v215, v216 op_sel_hi:[0,0,0] cbsz:4 blgp:2
	v_mfma_scale_f32_16x16x128_f8f6f4 v[116:119], v[156:159], v[166:171], v[116:119], v215, v217 op_sel_hi:[0,0,0] cbsz:4 blgp:2
	v_mfma_scale_f32_16x16x128_f8f6f4 v[120:123], v[156:159], v[172:177], v[120:123], v215, v218 op_sel_hi:[0,0,0] cbsz:4 blgp:2
	v_mfma_scale_f32_16x16x128_f8f6f4 v[124:127], v[156:159], v[178:183], v[124:127], v215, v219 op_sel_hi:[0,0,0] cbsz:4 blgp:2
	s_add_u32 s34, s34, 1
	s_waitcnt vmcnt(5)
	s_waitcnt lgkmcnt(0)
	s_barrier
	s_mul_i32 s35, s33, 0xa000
	v_add_u32_e32 v240, s35, v222
	v_add_u32_e32 v241, s35, v223
	v_add_u32_e32 v242, s35, v224
	s_add_u32 s33, s33, 1
	s_cmp_eq_u32 s33, 3
	s_cselect_b32 s33, 0, s33
	ds_read_b128 v[152:155], v240 offset:6144
	ds_read_b128 v[156:159], v240 offset:7168
	v_mfma_scale_f32_16x16x128_f8f6f4 v[0:3], v[128:131], v[184:189], v[0:3], v208, v216 op_sel_hi:[0,0,0] cbsz:4 blgp:2
	v_mfma_scale_f32_16x16x128_f8f6f4 v[4:7], v[128:131], v[190:195], v[4:7], v208, v217 op_sel_hi:[0,0,0] cbsz:4 blgp:2
	v_mfma_scale_f32_16x16x128_f8f6f4 v[8:11], v[128:131], v[196:201], v[8:11], v208, v218 op_sel_hi:[0,0,0] cbsz:4 blgp:2
	v_mfma_scale_f32_16x16x128_f8f6f4 v[12:15], v[128:131], v[202:207], v[12:15], v208, v219 op_sel_hi:[0,0,0] cbsz:4 blgp:2
	ds_read_b128 v[128:131], v240 offset:0
	ds_read_b128 v[160:163], v241 offset:0
	ds_read_b64 v[164:165], v242 offset:0
	v_mfma_scale_f32_16x16x128_f8f6f4 v[16:19], v[132:135], v[184:189], v[16:19], v209, v216 op_sel_hi:[0,0,0] cbsz:4 blgp:2
	v_mfma_scale_f32_16x16x128_f8f6f4 v[20:23], v[132:135], v[190:195], v[20:23], v209, v217 op_sel_hi:[0,0,0] cbsz:4 blgp:2
	v_mfma_scale_f32_16x16x128_f8f6f4 v[24:27], v[132:135], v[196:201], v[24:27], v209, v218 op_sel_hi:[0,0,0] cbsz:4 blgp:2
	v_mfma_scale_f32_16x16x128_f8f6f4 v[28:31], v[132:135], v[202:207], v[28:31], v209, v219 op_sel_hi:[0,0,0] cbsz:4 blgp:2
	s_cmp_eq_u32 s34, 13
	s_cselect_b32 s36, s38, s36
	s_cselect_b32 s37, s39, s37
	s_mov_b32 m0, s40
	ds_read_b128 v[132:135], v240 offset:1024
	ds_read_b128 v[166:169], v241 offset:1536
	ds_read_b64 v[170:171], v242 offset:1536
	buffer_load_dwordx4 v221, s[4:7], s36 offen lds
	v_mfma_scale_f32_16x16x128_f8f6f4 v[32:35], v[136:139], v[184:189], v[32:35], v210, v216 op_sel_hi:[0,0,0] cbsz:4 blgp:2
	v_mfma_scale_f32_16x16x128_f8f6f4 v[36:39], v[136:139], v[190:195], v[36:39], v210, v217 op_sel_hi:[0,0,0] cbsz:4 blgp:2
	v_mfma_scale_f32_16x16x128_f8f6f4 v[40:43], v[136:139], v[196:201], v[40:43], v210, v218 op_sel_hi:[0,0,0] cbsz:4 blgp:2
	v_mfma_scale_f32_16x16x128_f8f6f4 v[44:47], v[136:139], v[202:207], v[44:47], v210, v219 op_sel_hi:[0,0,0] cbsz:4 blgp:2
	s_add_u32 m0, s40, 0x2000
	ds_read_b128 v[136:139], v240 offset:2048
	ds_read_b128 v[172:175], v241 offset:3072
	ds_read_b64 v[176:177], v242 offset:3072
	buffer_load_dwordx4 v225, s[4:7], s36 offen lds
	v_mfma_scale_f32_16x16x128_f8f6f4 v[48:51], v[140:143], v[184:189], v[48:51], v211, v216 op_sel_hi:[0,0,0] cbsz:4 blgp:2
	v_mfma_scale_f32_16x16x128_f8f6f4 v[52:55], v[140:143], v[190:195], v[52:55], v211, v217 op_sel_hi:[0,0,0] cbsz:4 blgp:2
	v_mfma_scale_f32_16x16x128_f8f6f4 v[56:59], v[140:143], v[196:201], v[56:59], v211, v218 op_sel_hi:[0,0,0] cbsz:4 blgp:2
	v_mfma_scale_f32_16x16x128_f8f6f4 v[60:63], v[140:143], v[202:207], v[60:63], v211, v219 op_sel_hi:[0,0,0] cbsz:4 blgp:2
	s_add_u32 m0, s40, 0x4000
	ds_read_b128 v[140:143], v240 offset:3072
	ds_read_b128 v[178:181], v241 offset:4608
	ds_read_b64 v[182:183], v242 offset:4608
	buffer_load_dwordx4 v221, s[4:7], s37 offen lds
	v_mfma_scale_f32_16x16x128_f8f6f4 v[64:67], v[144:147], v[184:189], v[64:67], v212, v216 op_sel_hi:[0,0,0] cbsz:4 blgp:2
	v_mfma_scale_f32_16x16x128_f8f6f4 v[68:71], v[144:147], v[190:195], v[68:71], v212, v217 op_sel_hi:[0,0,0] cbsz:4 blgp:2
	v_mfma_scale_f32_16x16x128_f8f6f4 v[72:75], v[144:147], v[196:201], v[72:75], v212, v218 op_sel_hi:[0,0,0] cbsz:4 blgp:2
	v_mfma_scale_f32_16x16x128_f8f6f4 v[76:79], v[144:147], v[202:207], v[76:79], v212, v219 op_sel_hi:[0,0,0] cbsz:4 blgp:2
	s_add_u32 m0, s40, 0x6000
	ds_read_b128 v[144:147], v240 offset:4096
	buffer_load_dwordx4 v225, s[4:7], s37 offen lds
	v_mfma_scale_f32_16x16x128_f8f6f4 v[80:83], v[148:151], v[184:189], v[80:83], v213, v216 op_sel_hi:[0,0,0] cbsz:4 blgp:2
	v_mfma_scale_f32_16x16x128_f8f6f4 v[84:87], v[148:151], v[190:195], v[84:87], v213, v217 op_sel_hi:[0,0,0] cbsz:4 blgp:2
	v_mfma_scale_f32_16x16x128_f8f6f4 v[88:91], v[148:151], v[196:201], v[88:91], v213, v218 op_sel_hi:[0,0,0] cbsz:4 blgp:2
	v_mfma_scale_f32_16x16x128_f8f6f4 v[92:95], v[148:151], v[202:207], v[92:95], v213, v219 op_sel_hi:[0,0,0] cbsz:4 blgp:2
	s_add_u32 m0, s40, 0x8000
	ds_read_b128 v[148:151], v240 offset:5120
	buffer_load_dwordx4 v226, s[4:7], s37 offen lds
	s_add_u32 s36, s36, 0x4000
	s_add_u32 s37, s37, 0x6000
	s_add_u32 s40, s40, 0xa000
	s_sub_u32 s41, s40, 0x1e000
	s_cmp_ge_u32 s40, s49
	s_cselect_b32 s40, s41, s40
	v_mfma_scale_f32_16x16x128_f8f6f4 v[96:99], v[244:247], v[184:189], v[96:99], v214, v216 op_sel_hi:[0,0,0] cbsz:4 blgp:2
	v_mfma_scale_f32_16x16x128_f8f6f4 v[100:103], v[244:247], v[190:195], v[100:103], v214, v217 op_sel_hi:[0,0,0] cbsz:4 blgp:2
	v_mfma_scale_f32_16x16x128_f8f6f4 v[104:107], v[244:247], v[196:201], v[104:107], v214, v218 op_sel_hi:[0,0,0] cbsz:4 blgp:2
	v_mfma_scale_f32_16x16x128_f8f6f4 v[108:111], v[244:247], v[202:207], v[108:111], v214, v219 op_sel_hi:[0,0,0] cbsz:4 blgp:2
	s_cmp_eq_u32 s34, 13
	s_cbranch_scc0 .Lnosc_or0
	s_add_u32 s44, s23, 1
	s_and_b32 s44, s44, 1
	s_cmp_lt_u32 s18, 4
	s_cselect_b32 s80, s26, s27
	s_cselect_b32 s82, s8, s10
	s_cselect_b32 s83, s9, s11
	s_lshl_b32 s80, s80, 10
	s_and_b32 s84, s18, 3
	s_lshl_b32 s84, s84, 8
	s_add_u32 s80, s80, s84
	s_add_u32 s82, s82, s80
	s_addc_u32 s83, s83, 0
	s_lshl_b32 s84, s44, 11
	s_lshl_b32 s85, s18, 8
	s_add_u32 s84, s84, s85
	s_add_u32 s84, s84, 0x1e000
	s_mov_b32 m0, s84
	v_lshlrev_b32_e32 v236, 2, v220
	global_load_lds_dword v236, s[82:83]
.Lnosc_or0:
	v_mfma_scale_f32_16x16x128_f8f6f4 v[112:115], v[252:255], v[184:189], v[112:115], v215, v216 op_sel_hi:[0,0,0] cbsz:4 blgp:2
	v_mfma_scale_f32_16x16x128_f8f6f4 v[116:119], v[252:255], v[190:195], v[116:119], v215, v217 op_sel_hi:[0,0,0] cbsz:4 blgp:2
	v_mfma_scale_f32_16x16x128_f8f6f4 v[120:123], v[252:255], v[196:201], v[120:123], v215, v218 op_sel_hi:[0,0,0] cbsz:4 blgp:2
	v_mfma_scale_f32_16x16x128_f8f6f4 v[124:127], v[252:255], v[202:207], v[124:127], v215, v219 op_sel_hi:[0,0,0] cbsz:4 blgp:2
	s_add_u32 s34, s34, 1
	s_cmp_lt_u32 s34, 16
	s_cbranch_scc1 .Lkloop0
	s_add_u32 s44, s23, 1
	s_and_b32 s44, s44, 1
	s_lshl_b32 s80, s44, 11
	s_add_u32 s80, s80, 0x1e000
	s_lshl_b32 s82, s19, 9
	s_add_u32 s82, s82, s80
	s_lshl_b32 s83, s20, 8
	s_add_u32 s83, s83, s80
	s_add_u32 s83, s83, 0x400
	v_and_b32_e32 v234, 15, v220
	v_lshlrev_b32_e32 v234, 2, v234
	v_add_u32_e32 v235, s83, v234
	v_add_u32_e32 v234, s82, v234
	ds_read_b32 v208, v234 offset:0
	ds_read_b32 v209, v234 offset:64
	ds_read_b32 v210, v234 offset:128
	ds_read_b32 v211, v234 offset:192
	ds_read_b32 v212, v234 offset:256
	ds_read_b32 v213, v234 offset:320
	ds_read_b32 v214, v234 offset:384
	ds_read_b32 v215, v234 offset:448
	ds_read_b32 v216, v235 offset:0
	ds_read_b32 v217, v235 offset:64
	ds_read_b32 v218, v235 offset:128
	ds_read_b32 v219, v235 offset:192
	v_exp_f32_e32 v236, v0
	v_exp_f32_e32 v237, v1
	v_exp_f32_e32 v238, v2
	v_exp_f32_e32 v239, v3
	s_add_u32 s23, s23, 1
	v_exp_f32_e32 v240, v16
	v_exp_f32_e32 v241, v17
	v_exp_f32_e32 v242, v18
	v_exp_f32_e32 v243, v19
	s_mov_b32 s24, s26
	v_mov_b32_e32 v228, v236
	v_mov_b32_e32 v229, v237
	v_pk_add_f32 v[228:229], v[228:229], v[238:239]
	v_pk_add_f32 v[228:229], v[228:229], v[240:241]
	s_mov_b32 s25, s27
	v_pk_add_f32 v[228:229], v[228:229], v[242:243]
	v_exp_f32_e32 v236, v32
	v_exp_f32_e32 v237, v33
	v_exp_f32_e32 v238, v34
	s_mov_b32 s28, s30
	v_exp_f32_e32 v239, v35
	v_exp_f32_e32 v240, v48
	v_exp_f32_e32 v241, v49
	v_exp_f32_e32 v242, v50
	s_mov_b32 s29, s31
	v_exp_f32_e32 v243, v51
	v_pk_add_f32 v[228:229], v[228:229], v[236:237]
	v_pk_add_f32 v[228:229], v[228:229], v[238:239]
	v_pk_add_f32 v[228:229], v[228:229], v[240:241]
	s_add_u32 s45, s23, 1
	v_pk_add_f32 v[228:229], v[228:229], v[242:243]
	v_exp_f32_e32 v236, v64
	v_exp_f32_e32 v237, v65
	v_exp_f32_e32 v238, v66
	s_sub_u32 s46, s22, 1
	v_exp_f32_e32 v239, v67
	v_exp_f32_e32 v240, v80
	v_exp_f32_e32 v241, v81
	v_exp_f32_e32 v242, v82
	s_min_u32 s45, s45, s46
	v_exp_f32_e32 v243, v83
	v_pk_add_f32 v[228:229], v[228:229], v[236:237]
	v_pk_add_f32 v[228:229], v[228:229], v[238:239]
	v_pk_add_f32 v[228:229], v[228:229], v[240:241]
	s_lshl_b32 s45, s45, 5
	v_pk_add_f32 v[228:229], v[228:229], v[242:243]
	v_exp_f32_e32 v236, v96
	v_exp_f32_e32 v237, v97
	v_exp_f32_e32 v238, v98
	s_add_u32 s45, s45, s21
	v_exp_f32_e32 v239, v99
	v_exp_f32_e32 v240, v112
	v_exp_f32_e32 v241, v113
	v_exp_f32_e32 v242, v114
	s_lshr_b32 s80, s45, 5
	v_exp_f32_e32 v243, v115
	v_pk_add_f32 v[228:229], v[228:229], v[236:237]
	v_pk_add_f32 v[228:229], v[228:229], v[238:239]
	v_pk_add_f32 v[228:229], v[228:229], v[240:241]
	s_and_b32 s82, s45, 31
	v_pk_add_f32 v[228:229], v[228:229], v[242:243]
	v_exp_f32_e32 v236, v4
	v_exp_f32_e32 v237, v5
	v_exp_f32_e32 v238, v6
	s_lshr_b32 s83, s80, 1
	v_exp_f32_e32 v239, v7
	v_exp_f32_e32 v240, v20
	v_exp_f32_e32 v241, v21
	v_exp_f32_e32 v242, v22
	s_lshl_b32 s83, s83, 2
	v_exp_f32_e32 v243, v23
	v_mov_b32_e32 v230, v236
	v_mov_b32_e32 v231, v237
	v_pk_add_f32 v[230:231], v[230:231], v[238:239]
	s_lshr_b32 s84, s82, 3
	v_pk_add_f32 v[230:231], v[230:231], v[240:241]
	v_pk_add_f32 v[230:231], v[230:231], v[242:243]
	v_exp_f32_e32 v236, v36
	v_exp_f32_e32 v237, v37
	s_add_u32 s83, s83, s84
	v_exp_f32_e32 v238, v38
	v_exp_f32_e32 v239, v39
	v_exp_f32_e32 v240, v52
	v_exp_f32_e32 v241, v53
	s_and_b32 s84, s80, 1
	v_exp_f32_e32 v242, v54
	v_exp_f32_e32 v243, v55
	v_pk_add_f32 v[230:231], v[230:231], v[236:237]
	v_pk_add_f32 v[230:231], v[230:231], v[238:239]
	s_lshl_b32 s84, s84, 3
	v_pk_add_f32 v[230:231], v[230:231], v[240:241]
	v_pk_add_f32 v[230:231], v[230:231], v[242:243]
	v_exp_f32_e32 v236, v68
	v_exp_f32_e32 v237, v69
	s_and_b32 s85, s82, 7
	v_exp_f32_e32 v238, v70
	v_exp_f32_e32 v239, v71
	v_exp_f32_e32 v240, v84
	v_exp_f32_e32 v241, v85
	s_add_u32 s84, s84, s85
	v_exp_f32_e32 v242, v86
	v_exp_f32_e32 v243, v87
	v_pk_add_f32 v[230:231], v[230:231], v[236:237]
	v_pk_add_f32 v[230:231], v[230:231], v[238:239]
	s_sub_u32 s85, s45, 0x7c0
	v_pk_add_f32 v[230:231], v[230:231], v[240:241]
	v_pk_add_f32 v[230:231], v[230:231], v[242:243]
	v_exp_f32_e32 v236, v100
	v_exp_f32_e32 v237, v101
	s_cmpk_gt_u32 s45, 0x7bf
	v_exp_f32_e32 v238, v102
	v_exp_f32_e32 v239, v103
	v_exp_f32_e32 v240, v116
	v_exp_f32_e32 v241, v117
	s_cselect_b32 s26, 0x7c, s83
	v_exp_f32_e32 v242, v118
	v_exp_f32_e32 v243, v119
	v_pk_add_f32 v[230:231], v[230:231], v[236:237]
	v_pk_add_f32 v[230:231], v[230:231], v[238:239]
	s_cselect_b32 s27, s85, s84
	v_pk_add_f32 v[230:231], v[230:231], v[240:241]
	v_pk_add_f32 v[230:231], v[230:231], v[242:243]
	v_exp_f32_e32 v236, v8
	v_exp_f32_e32 v237, v9
	s_lshl_b32 s30, s26, 18
	v_exp_f32_e32 v238, v10
	v_exp_f32_e32 v239, v11
	v_exp_f32_e32 v240, v24
	v_exp_f32_e32 v241, v25
	s_mul_i32 s31, s27, 0x60000
	v_exp_f32_e32 v242, v26
	v_exp_f32_e32 v243, v27
	v_mov_b32_e32 v232, v236
	v_mov_b32_e32 v233, v237
	s_add_u32 s31, s31, 0x1f40000
	v_pk_add_f32 v[232:233], v[232:233], v[238:239]
	v_pk_add_f32 v[232:233], v[232:233], v[240:241]
	v_pk_add_f32 v[232:233], v[232:233], v[242:243]
	v_exp_f32_e32 v236, v40
	s_add_u32 s38, s30, s48
	v_exp_f32_e32 v237, v41
	v_exp_f32_e32 v238, v42
	v_exp_f32_e32 v239, v43
	v_exp_f32_e32 v240, v56
	s_add_u32 s39, s31, s48
	v_exp_f32_e32 v241, v57
	v_exp_f32_e32 v242, v58
	v_exp_f32_e32 v243, v59
	v_pk_add_f32 v[232:233], v[232:233], v[236:237]
	v_pk_add_f32 v[232:233], v[232:233], v[238:239]
	v_pk_add_f32 v[232:233], v[232:233], v[240:241]
	v_pk_add_f32 v[232:233], v[232:233], v[242:243]
	v_exp_f32_e32 v236, v72
	v_exp_f32_e32 v237, v73
	v_exp_f32_e32 v238, v74
	v_exp_f32_e32 v239, v75
	v_exp_f32_e32 v240, v88
	v_exp_f32_e32 v241, v89
	v_exp_f32_e32 v242, v90
	v_exp_f32_e32 v243, v91
	v_pk_add_f32 v[232:233], v[232:233], v[236:237]
	v_pk_add_f32 v[232:233], v[232:233], v[238:239]
	v_pk_add_f32 v[232:233], v[232:233], v[240:241]
	v_pk_add_f32 v[232:233], v[232:233], v[242:243]
	v_exp_f32_e32 v236, v104
	v_exp_f32_e32 v237, v105
	v_exp_f32_e32 v238, v106
	v_exp_f32_e32 v239, v107
	v_exp_f32_e32 v240, v120
	v_exp_f32_e32 v241, v121
	v_exp_f32_e32 v242, v122
	v_exp_f32_e32 v243, v123
	v_pk_add_f32 v[232:233], v[232:233], v[236:237]
	v_pk_add_f32 v[232:233], v[232:233], v[238:239]
	v_pk_add_f32 v[232:233], v[232:233], v[240:241]
	v_pk_add_f32 v[232:233], v[232:233], v[242:243]
	v_exp_f32_e32 v236, v12
	v_exp_f32_e32 v237, v13
	v_exp_f32_e32 v238, v14
	v_exp_f32_e32 v239, v15
	v_exp_f32_e32 v240, v28
	v_exp_f32_e32 v241, v29
	v_exp_f32_e32 v242, v30
	v_exp_f32_e32 v243, v31
	v_mov_b32_e32 v234, v236
	v_mov_b32_e32 v235, v237
	v_pk_add_f32 v[234:235], v[234:235], v[238:239]
	v_pk_add_f32 v[234:235], v[234:235], v[240:241]
	v_pk_add_f32 v[234:235], v[234:235], v[242:243]
	v_exp_f32_e32 v236, v44
	v_exp_f32_e32 v237, v45
	v_exp_f32_e32 v238, v46
	v_exp_f32_e32 v239, v47
	v_exp_f32_e32 v240, v60
	v_exp_f32_e32 v241, v61
	v_exp_f32_e32 v242, v62
	v_exp_f32_e32 v243, v63
	v_pk_add_f32 v[234:235], v[234:235], v[236:237]
	v_pk_add_f32 v[234:235], v[234:235], v[238:239]
	v_pk_add_f32 v[234:235], v[234:235], v[240:241]
	v_pk_add_f32 v[234:235], v[234:235], v[242:243]
	v_exp_f32_e32 v236, v76
	v_exp_f32_e32 v237, v77
	v_exp_f32_e32 v238, v78
	v_exp_f32_e32 v239, v79
	v_exp_f32_e32 v240, v92
	v_exp_f32_e32 v241, v93
	v_exp_f32_e32 v242, v94
	v_exp_f32_e32 v243, v95
	v_pk_add_f32 v[234:235], v[234:235], v[236:237]
	v_pk_add_f32 v[234:235], v[234:235], v[238:239]
	v_pk_add_f32 v[234:235], v[234:235], v[240:241]
	v_pk_add_f32 v[234:235], v[234:235], v[242:243]
	v_exp_f32_e32 v236, v108
	v_exp_f32_e32 v237, v109
	v_exp_f32_e32 v238, v110
	v_exp_f32_e32 v239, v111
	v_exp_f32_e32 v240, v124
	v_exp_f32_e32 v241, v125
	v_exp_f32_e32 v242, v126
	v_exp_f32_e32 v243, v127
	v_pk_add_f32 v[234:235], v[234:235], v[236:237]
	v_pk_add_f32 v[234:235], v[234:235], v[238:239]
	v_pk_add_f32 v[234:235], v[234:235], v[240:241]
	v_pk_add_f32 v[234:235], v[234:235], v[242:243]
	v_add_f32_e32 v228, v228, v229
	v_add_f32_e32 v230, v230, v231
	v_add_f32_e32 v232, v232, v233
	v_add_f32_e32 v234, v234, v235
	v_mov_b32_e32 v229, v228
	v_mov_b32_e32 v231, v230
	v_mov_b32_e32 v233, v232
	v_mov_b32_e32 v235, v234
	s_nop 1
	v_permlane16_swap_b32_e32 v228, v229
	v_permlane16_swap_b32_e32 v230, v231
	v_permlane16_swap_b32_e32 v232, v233
	v_permlane16_swap_b32_e32 v234, v235
	s_nop 1
	v_add_f32_e32 v228, v228, v229
	v_add_f32_e32 v230, v230, v231
	v_add_f32_e32 v232, v232, v233
	v_add_f32_e32 v234, v234, v235
	v_mov_b32_e32 v229, v228
	v_mov_b32_e32 v231, v230
	v_mov_b32_e32 v233, v232
	v_mov_b32_e32 v235, v234
	s_nop 1
	v_permlane32_swap_b32_e32 v228, v229
	v_permlane32_swap_b32_e32 v230, v231
	v_permlane32_swap_b32_e32 v232, v233
	v_permlane32_swap_b32_e32 v234, v235
	s_nop 1
	v_add_f32_e32 v228, v228, v229
	v_add_f32_e32 v230, v230, v231
	v_add_f32_e32 v232, v232, v233
	v_add_f32_e32 v234, v234, v235
	v_mov_b32_e32 v238, v228
	v_cndmask_b32_e64 v238, v238, v230, s[50:51]
	v_cndmask_b32_e64 v238, v238, v232, s[52:53]
	v_cndmask_b32_e64 v238, v238, v234, s[54:55]
	v_cmp_nle_f32_e64 s[60:61], s56, v238
	v_cmp_nge_f32_e64 s[58:59], s57, v238
	s_nop 3
	s_or_b64 s[58:59], s[58:59], s[60:61]
	s_cmp_lg_u64 s[58:59], 0
	s_cbranch_scc1 .Lslow0
	global_atomic_add_f32 v[248:249], v238, off
	s_branch .Lepi_done0
.Lslow0:
	v_max_f32_e32 v238, v0, v1
	v_max3_f32 v238, v238, v2, v3
	v_max3_f32 v238, v238, v16, v17
	v_max3_f32 v238, v238, v18, v19
	v_max3_f32 v238, v238, v32, v33
	v_max3_f32 v238, v238, v34, v35
	v_max3_f32 v238, v238, v48, v49
	v_max3_f32 v238, v238, v50, v51
	v_max3_f32 v238, v238, v64, v65
	v_max3_f32 v238, v238, v66, v67
	v_max3_f32 v238, v238, v80, v81
	v_max3_f32 v238, v238, v82, v83
	v_max3_f32 v238, v238, v96, v97
	v_max3_f32 v238, v238, v98, v99
	v_max3_f32 v238, v238, v112, v113
	v_max3_f32 v238, v238, v114, v115
	v_max_f32_e32 v239, v4, v5
	v_max3_f32 v239, v239, v6, v7
	v_max3_f32 v239, v239, v20, v21
	v_max3_f32 v239, v239, v22, v23
	v_max3_f32 v239, v239, v36, v37
	v_max3_f32 v239, v239, v38, v39
	v_max3_f32 v239, v239, v52, v53
	v_max3_f32 v239, v239, v54, v55
	v_max3_f32 v239, v239, v68, v69
	v_max3_f32 v239, v239, v70, v71
	v_max3_f32 v239, v239, v84, v85
	v_max3_f32 v239, v239, v86, v87
	v_max3_f32 v239, v239, v100, v101
	v_max3_f32 v239, v239, v102, v103
	v_max3_f32 v239, v239, v116, v117
	v_max3_f32 v239, v239, v118, v119
	v_max_f32_e32 v240, v8, v9
	v_max3_f32 v240, v240, v10, v11
	v_max3_f32 v240, v240, v24, v25
	v_max3_f32 v240, v240, v26, v27
	v_max3_f32 v240, v240, v40, v41
	v_max3_f32 v240, v240, v42, v43
	v_max3_f32 v240, v240, v56, v57
	v_max3_f32 v240, v240, v58, v59
	v_max3_f32 v240, v240, v72, v73
	v_max3_f32 v240, v240, v74, v75
	v_max3_f32 v240, v240, v88, v89
	v_max3_f32 v240, v240, v90, v91
	v_max3_f32 v240, v240, v104, v105
	v_max3_f32 v240, v240, v106, v107
	v_max3_f32 v240, v240, v120, v121
	v_max3_f32 v240, v240, v122, v123
	v_max_f32_e32 v241, v12, v13
	v_max3_f32 v241, v241, v14, v15
	v_max3_f32 v241, v241, v28, v29
	v_max3_f32 v241, v241, v30, v31
	v_max3_f32 v241, v241, v44, v45
	v_max3_f32 v241, v241, v46, v47
	v_max3_f32 v241, v241, v60, v61
	v_max3_f32 v241, v241, v62, v63
	v_max3_f32 v241, v241, v76, v77
	v_max3_f32 v241, v241, v78, v79
	v_max3_f32 v241, v241, v92, v93
	v_max3_f32 v241, v241, v94, v95
	v_max3_f32 v241, v241, v108, v109
	v_max3_f32 v241, v241, v110, v111
	v_max3_f32 v241, v241, v124, v125
	v_max3_f32 v241, v241, v126, v127
	v_mov_b32_e32 v229, v238
	v_mov_b32_e32 v231, v239
	v_mov_b32_e32 v233, v240
	v_mov_b32_e32 v235, v241
	s_nop 1
	v_permlane16_swap_b32_e32 v238, v229
	v_permlane16_swap_b32_e32 v239, v231
	v_permlane16_swap_b32_e32 v240, v233
	v_permlane16_swap_b32_e32 v241, v235
	s_nop 1
	v_max_f32_e32 v238, v238, v229
	v_max_f32_e32 v239, v239, v231
	v_max_f32_e32 v240, v240, v233
	v_max_f32_e32 v241, v241, v235
	v_mov_b32_e32 v229, v238
	v_mov_b32_e32 v231, v239
	v_mov_b32_e32 v233, v240
	v_mov_b32_e32 v235, v241
	s_nop 1
	v_permlane32_swap_b32_e32 v238, v229
	v_permlane32_swap_b32_e32 v239, v231
	v_permlane32_swap_b32_e32 v240, v233
	v_permlane32_swap_b32_e32 v241, v235
	s_nop 1
	v_max_f32_e32 v238, v238, v229
	v_max_f32_e32 v239, v239, v231
	v_max_f32_e32 v240, v240, v233
	v_max_f32_e32 v241, v241, v235
	v_mov_b32_e32 v228, 0
	v_sub_f32_e32 v242, v0, v238
	v_sub_f32_e32 v243, v1, v238
	v_exp_f32_e32 v242, v242
	v_exp_f32_e32 v243, v243
	s_nop 0
	v_add_f32_e32 v228, v228, v242
	v_add_f32_e32 v228, v228, v243
	v_sub_f32_e32 v242, v2, v238
	v_sub_f32_e32 v243, v3, v238
	v_exp_f32_e32 v242, v242
	v_exp_f32_e32 v243, v243
	s_nop 0
	v_add_f32_e32 v228, v228, v242
	v_add_f32_e32 v228, v228, v243
	v_sub_f32_e32 v242, v16, v238
	v_sub_f32_e32 v243, v17, v238
	v_exp_f32_e32 v242, v242
	v_exp_f32_e32 v243, v243
	s_nop 0
	v_add_f32_e32 v228, v228, v242
	v_add_f32_e32 v228, v228, v243
	v_sub_f32_e32 v242, v18, v238
	v_sub_f32_e32 v243, v19, v238
	v_exp_f32_e32 v242, v242
	v_exp_f32_e32 v243, v243
	s_nop 0
	v_add_f32_e32 v228, v228, v242
	v_add_f32_e32 v228, v228, v243
	v_sub_f32_e32 v242, v32, v238
	v_sub_f32_e32 v243, v33, v238
	v_exp_f32_e32 v242, v242
	v_exp_f32_e32 v243, v243
	s_nop 0
	v_add_f32_e32 v228, v228, v242
	v_add_f32_e32 v228, v228, v243
	v_sub_f32_e32 v242, v34, v238
	v_sub_f32_e32 v243, v35, v238
	v_exp_f32_e32 v242, v242
	v_exp_f32_e32 v243, v243
	s_nop 0
	v_add_f32_e32 v228, v228, v242
	v_add_f32_e32 v228, v228, v243
	v_sub_f32_e32 v242, v48, v238
	v_sub_f32_e32 v243, v49, v238
	v_exp_f32_e32 v242, v242
	v_exp_f32_e32 v243, v243
	s_nop 0
	v_add_f32_e32 v228, v228, v242
	v_add_f32_e32 v228, v228, v243
	v_sub_f32_e32 v242, v50, v238
	v_sub_f32_e32 v243, v51, v238
	v_exp_f32_e32 v242, v242
	v_exp_f32_e32 v243, v243
	s_nop 0
	v_add_f32_e32 v228, v228, v242
	v_add_f32_e32 v228, v228, v243
	v_sub_f32_e32 v242, v64, v238
	v_sub_f32_e32 v243, v65, v238
	v_exp_f32_e32 v242, v242
	v_exp_f32_e32 v243, v243
	s_nop 0
	v_add_f32_e32 v228, v228, v242
	v_add_f32_e32 v228, v228, v243
	v_sub_f32_e32 v242, v66, v238
	v_sub_f32_e32 v243, v67, v238
	v_exp_f32_e32 v242, v242
	v_exp_f32_e32 v243, v243
	s_nop 0
	v_add_f32_e32 v228, v228, v242
	v_add_f32_e32 v228, v228, v243
	v_sub_f32_e32 v242, v80, v238
	v_sub_f32_e32 v243, v81, v238
	v_exp_f32_e32 v242, v242
	v_exp_f32_e32 v243, v243
	s_nop 0
	v_add_f32_e32 v228, v228, v242
	v_add_f32_e32 v228, v228, v243
	v_sub_f32_e32 v242, v82, v238
	v_sub_f32_e32 v243, v83, v238
	v_exp_f32_e32 v242, v242
	v_exp_f32_e32 v243, v243
	s_nop 0
	v_add_f32_e32 v228, v228, v242
	v_add_f32_e32 v228, v228, v243
	v_sub_f32_e32 v242, v96, v238
	v_sub_f32_e32 v243, v97, v238
	v_exp_f32_e32 v242, v242
	v_exp_f32_e32 v243, v243
	s_nop 0
	v_add_f32_e32 v228, v228, v242
	v_add_f32_e32 v228, v228, v243
	v_sub_f32_e32 v242, v98, v238
	v_sub_f32_e32 v243, v99, v238
	v_exp_f32_e32 v242, v242
	v_exp_f32_e32 v243, v243
	s_nop 0
	v_add_f32_e32 v228, v228, v242
	v_add_f32_e32 v228, v228, v243
	v_sub_f32_e32 v242, v112, v238
	v_sub_f32_e32 v243, v113, v238
	v_exp_f32_e32 v242, v242
	v_exp_f32_e32 v243, v243
	s_nop 0
	v_add_f32_e32 v228, v228, v242
	v_add_f32_e32 v228, v228, v243
	v_sub_f32_e32 v242, v114, v238
	v_sub_f32_e32 v243, v115, v238
	v_exp_f32_e32 v242, v242
	v_exp_f32_e32 v243, v243
	s_nop 0
	v_add_f32_e32 v228, v228, v242
	v_add_f32_e32 v228, v228, v243
	v_mov_b32_e32 v230, 0
	v_sub_f32_e32 v242, v4, v239
	v_sub_f32_e32 v243, v5, v239
	v_exp_f32_e32 v242, v242
	v_exp_f32_e32 v243, v243
	s_nop 0
	v_add_f32_e32 v230, v230, v242
	v_add_f32_e32 v230, v230, v243
	v_sub_f32_e32 v242, v6, v239
	v_sub_f32_e32 v243, v7, v239
	v_exp_f32_e32 v242, v242
	v_exp_f32_e32 v243, v243
	s_nop 0
	v_add_f32_e32 v230, v230, v242
	v_add_f32_e32 v230, v230, v243
	v_sub_f32_e32 v242, v20, v239
	v_sub_f32_e32 v243, v21, v239
	v_exp_f32_e32 v242, v242
	v_exp_f32_e32 v243, v243
	s_nop 0
	v_add_f32_e32 v230, v230, v242
	v_add_f32_e32 v230, v230, v243
	v_sub_f32_e32 v242, v22, v239
	v_sub_f32_e32 v243, v23, v239
	v_exp_f32_e32 v242, v242
	v_exp_f32_e32 v243, v243
	s_nop 0
	v_add_f32_e32 v230, v230, v242
	v_add_f32_e32 v230, v230, v243
	v_sub_f32_e32 v242, v36, v239
	v_sub_f32_e32 v243, v37, v239
	v_exp_f32_e32 v242, v242
	v_exp_f32_e32 v243, v243
	s_nop 0
	v_add_f32_e32 v230, v230, v242
	v_add_f32_e32 v230, v230, v243
	v_sub_f32_e32 v242, v38, v239
	v_sub_f32_e32 v243, v39, v239
	v_exp_f32_e32 v242, v242
	v_exp_f32_e32 v243, v243
	s_nop 0
	v_add_f32_e32 v230, v230, v242
	v_add_f32_e32 v230, v230, v243
	v_sub_f32_e32 v242, v52, v239
	v_sub_f32_e32 v243, v53, v239
	v_exp_f32_e32 v242, v242
	v_exp_f32_e32 v243, v243
	s_nop 0
	v_add_f32_e32 v230, v230, v242
	v_add_f32_e32 v230, v230, v243
	v_sub_f32_e32 v242, v54, v239
	v_sub_f32_e32 v243, v55, v239
	v_exp_f32_e32 v242, v242
	v_exp_f32_e32 v243, v243
	s_nop 0
	v_add_f32_e32 v230, v230, v242
	v_add_f32_e32 v230, v230, v243
	v_sub_f32_e32 v242, v68, v239
	v_sub_f32_e32 v243, v69, v239
	v_exp_f32_e32 v242, v242
	v_exp_f32_e32 v243, v243
	s_nop 0
	v_add_f32_e32 v230, v230, v242
	v_add_f32_e32 v230, v230, v243
	v_sub_f32_e32 v242, v70, v239
	v_sub_f32_e32 v243, v71, v239
	v_exp_f32_e32 v242, v242
	v_exp_f32_e32 v243, v243
	s_nop 0
	v_add_f32_e32 v230, v230, v242
	v_add_f32_e32 v230, v230, v243
	v_sub_f32_e32 v242, v84, v239
	v_sub_f32_e32 v243, v85, v239
	v_exp_f32_e32 v242, v242
	v_exp_f32_e32 v243, v243
	s_nop 0
	v_add_f32_e32 v230, v230, v242
	v_add_f32_e32 v230, v230, v243
	v_sub_f32_e32 v242, v86, v239
	v_sub_f32_e32 v243, v87, v239
	v_exp_f32_e32 v242, v242
	v_exp_f32_e32 v243, v243
	s_nop 0
	v_add_f32_e32 v230, v230, v242
	v_add_f32_e32 v230, v230, v243
	v_sub_f32_e32 v242, v100, v239
	v_sub_f32_e32 v243, v101, v239
	v_exp_f32_e32 v242, v242
	v_exp_f32_e32 v243, v243
	s_nop 0
	v_add_f32_e32 v230, v230, v242
	v_add_f32_e32 v230, v230, v243
	v_sub_f32_e32 v242, v102, v239
	v_sub_f32_e32 v243, v103, v239
	v_exp_f32_e32 v242, v242
	v_exp_f32_e32 v243, v243
	s_nop 0
	v_add_f32_e32 v230, v230, v242
	v_add_f32_e32 v230, v230, v243
	v_sub_f32_e32 v242, v116, v239
	v_sub_f32_e32 v243, v117, v239
	v_exp_f32_e32 v242, v242
	v_exp_f32_e32 v243, v243
	s_nop 0
	v_add_f32_e32 v230, v230, v242
	v_add_f32_e32 v230, v230, v243
	v_sub_f32_e32 v242, v118, v239
	v_sub_f32_e32 v243, v119, v239
	v_exp_f32_e32 v242, v242
	v_exp_f32_e32 v243, v243
	s_nop 0
	v_add_f32_e32 v230, v230, v242
	v_add_f32_e32 v230, v230, v243
	v_mov_b32_e32 v232, 0
	v_sub_f32_e32 v242, v8, v240
	v_sub_f32_e32 v243, v9, v240
	v_exp_f32_e32 v242, v242
	v_exp_f32_e32 v243, v243
	s_nop 0
	v_add_f32_e32 v232, v232, v242
	v_add_f32_e32 v232, v232, v243
	v_sub_f32_e32 v242, v10, v240
	v_sub_f32_e32 v243, v11, v240
	v_exp_f32_e32 v242, v242
	v_exp_f32_e32 v243, v243
	s_nop 0
	v_add_f32_e32 v232, v232, v242
	v_add_f32_e32 v232, v232, v243
	v_sub_f32_e32 v242, v24, v240
	v_sub_f32_e32 v243, v25, v240
	v_exp_f32_e32 v242, v242
	v_exp_f32_e32 v243, v243
	s_nop 0
	v_add_f32_e32 v232, v232, v242
	v_add_f32_e32 v232, v232, v243
	v_sub_f32_e32 v242, v26, v240
	v_sub_f32_e32 v243, v27, v240
	v_exp_f32_e32 v242, v242
	v_exp_f32_e32 v243, v243
	s_nop 0
	v_add_f32_e32 v232, v232, v242
	v_add_f32_e32 v232, v232, v243
	v_sub_f32_e32 v242, v40, v240
	v_sub_f32_e32 v243, v41, v240
	v_exp_f32_e32 v242, v242
	v_exp_f32_e32 v243, v243
	s_nop 0
	v_add_f32_e32 v232, v232, v242
	v_add_f32_e32 v232, v232, v243
	v_sub_f32_e32 v242, v42, v240
	v_sub_f32_e32 v243, v43, v240
	v_exp_f32_e32 v242, v242
	v_exp_f32_e32 v243, v243
	s_nop 0
	v_add_f32_e32 v232, v232, v242
	v_add_f32_e32 v232, v232, v243
	v_sub_f32_e32 v242, v56, v240
	v_sub_f32_e32 v243, v57, v240
	v_exp_f32_e32 v242, v242
	v_exp_f32_e32 v243, v243
	s_nop 0
	v_add_f32_e32 v232, v232, v242
	v_add_f32_e32 v232, v232, v243
	v_sub_f32_e32 v242, v58, v240
	v_sub_f32_e32 v243, v59, v240
	v_exp_f32_e32 v242, v242
	v_exp_f32_e32 v243, v243
	s_nop 0
	v_add_f32_e32 v232, v232, v242
	v_add_f32_e32 v232, v232, v243
	v_sub_f32_e32 v242, v72, v240
	v_sub_f32_e32 v243, v73, v240
	v_exp_f32_e32 v242, v242
	v_exp_f32_e32 v243, v243
	s_nop 0
	v_add_f32_e32 v232, v232, v242
	v_add_f32_e32 v232, v232, v243
	v_sub_f32_e32 v242, v74, v240
	v_sub_f32_e32 v243, v75, v240
	v_exp_f32_e32 v242, v242
	v_exp_f32_e32 v243, v243
	s_nop 0
	v_add_f32_e32 v232, v232, v242
	v_add_f32_e32 v232, v232, v243
	v_sub_f32_e32 v242, v88, v240
	v_sub_f32_e32 v243, v89, v240
	v_exp_f32_e32 v242, v242
	v_exp_f32_e32 v243, v243
	s_nop 0
	v_add_f32_e32 v232, v232, v242
	v_add_f32_e32 v232, v232, v243
	v_sub_f32_e32 v242, v90, v240
	v_sub_f32_e32 v243, v91, v240
	v_exp_f32_e32 v242, v242
	v_exp_f32_e32 v243, v243
	s_nop 0
	v_add_f32_e32 v232, v232, v242
	v_add_f32_e32 v232, v232, v243
	v_sub_f32_e32 v242, v104, v240
	v_sub_f32_e32 v243, v105, v240
	v_exp_f32_e32 v242, v242
	v_exp_f32_e32 v243, v243
	s_nop 0
	v_add_f32_e32 v232, v232, v242
	v_add_f32_e32 v232, v232, v243
	v_sub_f32_e32 v242, v106, v240
	v_sub_f32_e32 v243, v107, v240
	v_exp_f32_e32 v242, v242
	v_exp_f32_e32 v243, v243
	s_nop 0
	v_add_f32_e32 v232, v232, v242
	v_add_f32_e32 v232, v232, v243
	v_sub_f32_e32 v242, v120, v240
	v_sub_f32_e32 v243, v121, v240
	v_exp_f32_e32 v242, v242
	v_exp_f32_e32 v243, v243
	s_nop 0
	v_add_f32_e32 v232, v232, v242
	v_add_f32_e32 v232, v232, v243
	v_sub_f32_e32 v242, v122, v240
	v_sub_f32_e32 v243, v123, v240
	v_exp_f32_e32 v242, v242
	v_exp_f32_e32 v243, v243
	s_nop 0
	v_add_f32_e32 v232, v232, v242
	v_add_f32_e32 v232, v232, v243
	v_mov_b32_e32 v234, 0
	v_sub_f32_e32 v242, v12, v241
	v_sub_f32_e32 v243, v13, v241
	v_exp_f32_e32 v242, v242
	v_exp_f32_e32 v243, v243
	s_nop 0
	v_add_f32_e32 v234, v234, v242
	v_add_f32_e32 v234, v234, v243
	v_sub_f32_e32 v242, v14, v241
	v_sub_f32_e32 v243, v15, v241
	v_exp_f32_e32 v242, v242
	v_exp_f32_e32 v243, v243
	s_nop 0
	v_add_f32_e32 v234, v234, v242
	v_add_f32_e32 v234, v234, v243
	v_sub_f32_e32 v242, v28, v241
	v_sub_f32_e32 v243, v29, v241
	v_exp_f32_e32 v242, v242
	v_exp_f32_e32 v243, v243
	s_nop 0
	v_add_f32_e32 v234, v234, v242
	v_add_f32_e32 v234, v234, v243
	v_sub_f32_e32 v242, v30, v241
	v_sub_f32_e32 v243, v31, v241
	v_exp_f32_e32 v242, v242
	v_exp_f32_e32 v243, v243
	s_nop 0
	v_add_f32_e32 v234, v234, v242
	v_add_f32_e32 v234, v234, v243
	v_sub_f32_e32 v242, v44, v241
	v_sub_f32_e32 v243, v45, v241
	v_exp_f32_e32 v242, v242
	v_exp_f32_e32 v243, v243
	s_nop 0
	v_add_f32_e32 v234, v234, v242
	v_add_f32_e32 v234, v234, v243
	v_sub_f32_e32 v242, v46, v241
	v_sub_f32_e32 v243, v47, v241
	v_exp_f32_e32 v242, v242
	v_exp_f32_e32 v243, v243
	s_nop 0
	v_add_f32_e32 v234, v234, v242
	v_add_f32_e32 v234, v234, v243
	v_sub_f32_e32 v242, v60, v241
	v_sub_f32_e32 v243, v61, v241
	v_exp_f32_e32 v242, v242
	v_exp_f32_e32 v243, v243
	s_nop 0
	v_add_f32_e32 v234, v234, v242
	v_add_f32_e32 v234, v234, v243
	v_sub_f32_e32 v242, v62, v241
	v_sub_f32_e32 v243, v63, v241
	v_exp_f32_e32 v242, v242
	v_exp_f32_e32 v243, v243
	s_nop 0
	v_add_f32_e32 v234, v234, v242
	v_add_f32_e32 v234, v234, v243
	v_sub_f32_e32 v242, v76, v241
	v_sub_f32_e32 v243, v77, v241
	v_exp_f32_e32 v242, v242
	v_exp_f32_e32 v243, v243
	s_nop 0
	v_add_f32_e32 v234, v234, v242
	v_add_f32_e32 v234, v234, v243
	v_sub_f32_e32 v242, v78, v241
	v_sub_f32_e32 v243, v79, v241
	v_exp_f32_e32 v242, v242
	v_exp_f32_e32 v243, v243
	s_nop 0
	v_add_f32_e32 v234, v234, v242
	v_add_f32_e32 v234, v234, v243
	v_sub_f32_e32 v242, v92, v241
	v_sub_f32_e32 v243, v93, v241
	v_exp_f32_e32 v242, v242
	v_exp_f32_e32 v243, v243
	s_nop 0
	v_add_f32_e32 v234, v234, v242
	v_add_f32_e32 v234, v234, v243
	v_sub_f32_e32 v242, v94, v241
	v_sub_f32_e32 v243, v95, v241
	v_exp_f32_e32 v242, v242
	v_exp_f32_e32 v243, v243
	s_nop 0
	v_add_f32_e32 v234, v234, v242
	v_add_f32_e32 v234, v234, v243
	v_sub_f32_e32 v242, v108, v241
	v_sub_f32_e32 v243, v109, v241
	v_exp_f32_e32 v242, v242
	v_exp_f32_e32 v243, v243
	s_nop 0
	v_add_f32_e32 v234, v234, v242
	v_add_f32_e32 v234, v234, v243
	v_sub_f32_e32 v242, v110, v241
	v_sub_f32_e32 v243, v111, v241
	v_exp_f32_e32 v242, v242
	v_exp_f32_e32 v243, v243
	s_nop 0
	v_add_f32_e32 v234, v234, v242
	v_add_f32_e32 v234, v234, v243
	v_sub_f32_e32 v242, v124, v241
	v_sub_f32_e32 v243, v125, v241
	v_exp_f32_e32 v242, v242
	v_exp_f32_e32 v243, v243
	s_nop 0
	v_add_f32_e32 v234, v234, v242
	v_add_f32_e32 v234, v234, v243
	v_sub_f32_e32 v242, v126, v241
	v_sub_f32_e32 v243, v127, v241
	v_exp_f32_e32 v242, v242
	v_exp_f32_e32 v243, v243
	s_nop 0
	v_add_f32_e32 v234, v234, v242
	v_add_f32_e32 v234, v234, v243
	v_mov_b32_e32 v229, v228
	v_mov_b32_e32 v231, v230
	v_mov_b32_e32 v233, v232
	v_mov_b32_e32 v235, v234
	s_nop 1
	v_permlane16_swap_b32_e32 v228, v229
	v_permlane16_swap_b32_e32 v230, v231
	v_permlane16_swap_b32_e32 v232, v233
	v_permlane16_swap_b32_e32 v234, v235
	s_nop 1
	v_add_f32_e32 v228, v228, v229
	v_add_f32_e32 v230, v230, v231
	v_add_f32_e32 v232, v232, v233
	v_add_f32_e32 v234, v234, v235
	v_mov_b32_e32 v229, v228
	v_mov_b32_e32 v231, v230
	v_mov_b32_e32 v233, v232
	v_mov_b32_e32 v235, v234
	s_nop 1
	v_permlane32_swap_b32_e32 v228, v229
	v_permlane32_swap_b32_e32 v230, v231
	v_permlane32_swap_b32_e32 v232, v233
	v_permlane32_swap_b32_e32 v234, v235
	s_nop 1
	v_add_f32_e32 v228, v228, v229
	v_add_f32_e32 v230, v230, v231
	v_add_f32_e32 v232, v232, v233
	v_add_f32_e32 v234, v234, v235
	v_mov_b32_e32 v236, v238
	v_cndmask_b32_e64 v236, v236, v239, s[50:51]
	v_cndmask_b32_e64 v236, v236, v240, s[52:53]
	v_cndmask_b32_e64 v236, v236, v241, s[54:55]
	v_mov_b32_e32 v237, v228
	v_cndmask_b32_e64 v237, v237, v230, s[50:51]
	v_cndmask_b32_e64 v237, v237, v232, s[52:53]
	v_cndmask_b32_e64 v237, v237, v234, s[54:55]
	v_lshl_add_u64 v[238:239], v[250:251], 2, s[14:15]
	v_mov_b32_e32 v240, 1
	global_atomic_add v241, v[238:239], v240, off sc0
	v_mul_u32_u24_e32 v242, 0xfa, v250
	v_mov_b32_e32 v243, 0
	s_waitcnt vmcnt(0)
	v_add_u32_e32 v242, v242, v241
	v_lshl_add_u64 v[238:239], v[242:243], 3, s[16:17]
	global_store_dwordx2 v[238:239], v[236:237], off
.Lepi_done0:
	s_cmp_eq_u32 s23, s22
	s_cbranch_scc1 .Lexit
	s_lshl_b32 s80, s25, 8
	s_lshl_b32 s82, s20, 6
	s_add_u32 s80, s80, s82
	v_add_u32_e32 v250, s80, v220
	v_lshl_add_u64 v[248:249], v[250:251], 2, s[12:13]
	s_branch .Ltile0
.Ltile1:
	s_mov_b32 s34, 0
	s_waitcnt vmcnt(5)
	s_waitcnt lgkmcnt(0)
	s_barrier
	s_mul_i32 s35, s33, 0xa000
	v_add_u32_e32 v240, s35, v222
	v_add_u32_e32 v241, s35, v223
	v_add_u32_e32 v242, s35, v224
	s_add_u32 s33, s33, 1
	s_cmp_eq_u32 s33, 3
	s_cselect_b32 s33, 0, s33
	ds_read_b128 v[244:247], v240 offset:6144
	ds_read_b128 v[252:255], v240 offset:7168
	v_mfma_scale_f32_16x16x128_f8f6f4 v[0:3], v[128:131], v[160:165], 0, v208, v216 op_sel_hi:[0,0,0] cbsz:4 blgp:2
	v_mfma_scale_f32_16x16x128_f8f6f4 v[4:7], v[128:131], v[166:171], 0, v208, v217 op_sel_hi:[0,0,0] cbsz:4 blgp:2
	v_mfma_scale_f32_16x16x128_f8f6f4 v[8:11], v[128:131], v[172:177], 0, v208, v218 op_sel_hi:[0,0,0] cbsz:4 blgp:2
	v_mfma_scale_f32_16x16x128_f8f6f4 v[12:15], v[128:131], v[178:183], 0, v208, v219 op_sel_hi:[0,0,0] cbsz:4 blgp:2
	v_mfma_scale_f32_16x16x128_f8f6f4 v[16:19], v[132:135], v[160:165], 0, v209, v216 op_sel_hi:[0,0,0] cbsz:4 blgp:2
	v_mfma_scale_f32_16x16x128_f8f6f4 v[20:23], v[132:135], v[166:171], 0, v209, v217 op_sel_hi:[0,0,0] cbsz:4 blgp:2
	ds_read_b128 v[128:131], v240 offset:0
	ds_read_b128 v[184:187], v241 offset:0
	ds_read_b64 v[188:189], v242 offset:0
	v_mfma_scale_f32_16x16x128_f8f6f4 v[24:27], v[132:135], v[172:177], 0, v209, v218 op_sel_hi:[0,0,0] cbsz:4 blgp:2
	v_mfma_scale_f32_16x16x128_f8f6f4 v[28:31], v[132:135], v[178:183], 0, v209, v219 op_sel_hi:[0,0,0] cbsz:4 blgp:2
	v_mfma_scale_f32_16x16x128_f8f6f4 v[32:35], v[136:139], v[160:165], 0, v210, v216 op_sel_hi:[0,0,0] cbsz:4 blgp:2
	v_mfma_scale_f32_16x16x128_f8f6f4 v[36:39], v[136:139], v[166:171], 0, v210, v217 op_sel_hi:[0,0,0] cbsz:4 blgp:2
	s_cmp_eq_u32 s34, 13
	s_cselect_b32 s36, s38, s36
	s_cselect_b32 s37, s39, s37
	s_mov_b32 m0, s40
	ds_read_b128 v[132:135], v240 offset:1024
	ds_read_b128 v[190:193], v241 offset:1536
	ds_read_b64 v[194:195], v242 offset:1536
	buffer_load_dwordx4 v221, s[4:7], s36 offen lds
	v_mfma_scale_f32_16x16x128_f8f6f4 v[40:43], v[136:139], v[172:177], 0, v210, v218 op_sel_hi:[0,0,0] cbsz:4 blgp:2
	v_mfma_scale_f32_16x16x128_f8f6f4 v[44:47], v[136:139], v[178:183], 0, v210, v219 op_sel_hi:[0,0,0] cbsz:4 blgp:2
	v_mfma_scale_f32_16x16x128_f8f6f4 v[48:51], v[140:143], v[160:165], 0, v211, v216 op_sel_hi:[0,0,0] cbsz:4 blgp:2
	v_mfma_scale_f32_16x16x128_f8f6f4 v[52:55], v[140:143], v[166:171], 0, v211, v217 op_sel_hi:[0,0,0] cbsz:4 blgp:2
	s_add_u32 m0, s40, 0x2000
	ds_read_b128 v[136:139], v240 offset:2048
	ds_read_b128 v[196:199], v241 offset:3072
	ds_read_b64 v[200:201], v242 offset:3072
	buffer_load_dwordx4 v225, s[4:7], s36 offen lds
	v_mfma_scale_f32_16x16x128_f8f6f4 v[56:59], v[140:143], v[172:177], 0, v211, v218 op_sel_hi:[0,0,0] cbsz:4 blgp:2
	v_mfma_scale_f32_16x16x128_f8f6f4 v[60:63], v[140:143], v[178:183], 0, v211, v219 op_sel_hi:[0,0,0] cbsz:4 blgp:2
	v_mfma_scale_f32_16x16x128_f8f6f4 v[64:67], v[144:147], v[160:165], 0, v212, v216 op_sel_hi:[0,0,0] cbsz:4 blgp:2
	v_mfma_scale_f32_16x16x128_f8f6f4 v[68:71], v[144:147], v[166:171], 0, v212, v217 op_sel_hi:[0,0,0] cbsz:4 blgp:2
	s_add_u32 m0, s40, 0x4000
	ds_read_b128 v[140:143], v240 offset:3072
	ds_read_b128 v[202:205], v241 offset:4608
	ds_read_b64 v[206:207], v242 offset:4608
	buffer_load_dwordx4 v221, s[4:7], s37 offen lds
	v_mfma_scale_f32_16x16x128_f8f6f4 v[72:75], v[144:147], v[172:177], 0, v212, v218 op_sel_hi:[0,0,0] cbsz:4 blgp:2
	v_mfma_scale_f32_16x16x128_f8f6f4 v[76:79], v[144:147], v[178:183], 0, v212, v219 op_sel_hi:[0,0,0] cbsz:4 blgp:2
	v_mfma_scale_f32_16x16x128_f8f6f4 v[80:83], v[148:151], v[160:165], 0, v213, v216 op_sel_hi:[0,0,0] cbsz:4 blgp:2
	v_mfma_scale_f32_16x16x128_f8f6f4 v[84:87], v[148:151], v[166:171], 0, v213, v217 op_sel_hi:[0,0,0] cbsz:4 blgp:2
	s_add_u32 m0, s40, 0x6000
	ds_read_b128 v[144:147], v240 offset:4096
	buffer_load_dwordx4 v225, s[4:7], s37 offen lds
	v_mfma_scale_f32_16x16x128_f8f6f4 v[88:91], v[148:151], v[172:177], 0, v213, v218 op_sel_hi:[0,0,0] cbsz:4 blgp:2
	v_mfma_scale_f32_16x16x128_f8f6f4 v[92:95], v[148:151], v[178:183], 0, v213, v219 op_sel_hi:[0,0,0] cbsz:4 blgp:2
	v_mfma_scale_f32_16x16x128_f8f6f4 v[96:99], v[152:155], v[160:165], 0, v214, v216 op_sel_hi:[0,0,0] cbsz:4 blgp:2
	v_mfma_scale_f32_16x16x128_f8f6f4 v[100:103], v[152:155], v[166:171], 0, v214, v217 op_sel_hi:[0,0,0] cbsz:4 blgp:2
	s_add_u32 m0, s40, 0x8000
	ds_read_b128 v[148:151], v240 offset:5120
	buffer_load_dwordx4 v226, s[4:7], s37 offen lds
	s_add_u32 s36, s36, 0x4000
	s_add_u32 s37, s37, 0x6000
	s_add_u32 s40, s40, 0xa000
	s_sub_u32 s41, s40, 0x1e000
	s_cmp_ge_u32 s40, s49
	s_cselect_b32 s40, s41, s40
	v_mfma_scale_f32_16x16x128_f8f6f4 v[104:107], v[152:155], v[172:177], 0, v214, v218 op_sel_hi:[0,0,0] cbsz:4 blgp:2
	v_mfma_scale_f32_16x16x128_f8f6f4 v[108:111], v[152:155], v[178:183], 0, v214, v219 op_sel_hi:[0,0,0] cbsz:4 blgp:2
	v_mfma_scale_f32_16x16x128_f8f6f4 v[112:115], v[156:159], v[160:165], 0, v215, v216 op_sel_hi:[0,0,0] cbsz:4 blgp:2
	v_mfma_scale_f32_16x16x128_f8f6f4 v[116:119], v[156:159], v[166:171], 0, v215, v217 op_sel_hi:[0,0,0] cbsz:4 blgp:2
	v_mfma_scale_f32_16x16x128_f8f6f4 v[120:123], v[156:159], v[172:177], 0, v215, v218 op_sel_hi:[0,0,0] cbsz:4 blgp:2
	v_mfma_scale_f32_16x16x128_f8f6f4 v[124:127], v[156:159], v[178:183], 0, v215, v219 op_sel_hi:[0,0,0] cbsz:4 blgp:2
	s_add_u32 s34, s34, 1
	s_waitcnt vmcnt(5)
	s_waitcnt lgkmcnt(0)
	s_barrier
	s_mul_i32 s35, s33, 0xa000
	v_add_u32_e32 v240, s35, v222
	v_add_u32_e32 v241, s35, v223
	v_add_u32_e32 v242, s35, v224
	s_add_u32 s33, s33, 1
	s_cmp_eq_u32 s33, 3
	s_cselect_b32 s33, 0, s33
	ds_read_b128 v[152:155], v240 offset:6144
	ds_read_b128 v[156:159], v240 offset:7168
	v_mfma_scale_f32_16x16x128_f8f6f4 v[0:3], v[128:131], v[184:189], v[0:3], v208, v216 op_sel_hi:[0,0,0] cbsz:4 blgp:2
	v_mfma_scale_f32_16x16x128_f8f6f4 v[4:7], v[128:131], v[190:195], v[4:7], v208, v217 op_sel_hi:[0,0,0] cbsz:4 blgp:2
	v_mfma_scale_f32_16x16x128_f8f6f4 v[8:11], v[128:131], v[196:201], v[8:11], v208, v218 op_sel_hi:[0,0,0] cbsz:4 blgp:2
	v_mfma_scale_f32_16x16x128_f8f6f4 v[12:15], v[128:131], v[202:207], v[12:15], v208, v219 op_sel_hi:[0,0,0] cbsz:4 blgp:2
	v_mfma_scale_f32_16x16x128_f8f6f4 v[16:19], v[132:135], v[184:189], v[16:19], v209, v216 op_sel_hi:[0,0,0] cbsz:4 blgp:2
	v_mfma_scale_f32_16x16x128_f8f6f4 v[20:23], v[132:135], v[190:195], v[20:23], v209, v217 op_sel_hi:[0,0,0] cbsz:4 blgp:2
	ds_read_b128 v[128:131], v240 offset:0
	ds_read_b128 v[160:163], v241 offset:0
	ds_read_b64 v[164:165], v242 offset:0
	v_mfma_scale_f32_16x16x128_f8f6f4 v[24:27], v[132:135], v[196:201], v[24:27], v209, v218 op_sel_hi:[0,0,0] cbsz:4 blgp:2
	v_mfma_scale_f32_16x16x128_f8f6f4 v[28:31], v[132:135], v[202:207], v[28:31], v209, v219 op_sel_hi:[0,0,0] cbsz:4 blgp:2
	v_mfma_scale_f32_16x16x128_f8f6f4 v[32:35], v[136:139], v[184:189], v[32:35], v210, v216 op_sel_hi:[0,0,0] cbsz:4 blgp:2
	v_mfma_scale_f32_16x16x128_f8f6f4 v[36:39], v[136:139], v[190:195], v[36:39], v210, v217 op_sel_hi:[0,0,0] cbsz:4 blgp:2
	s_cmp_eq_u32 s34, 13
	s_cselect_b32 s36, s38, s36
	s_cselect_b32 s37, s39, s37
	s_mov_b32 m0, s40
	ds_read_b128 v[132:135], v240 offset:1024
	ds_read_b128 v[166:169], v241 offset:1536
	ds_read_b64 v[170:171], v242 offset:1536
	buffer_load_dwordx4 v221, s[4:7], s36 offen lds
	v_mfma_scale_f32_16x16x128_f8f6f4 v[40:43], v[136:139], v[196:201], v[40:43], v210, v218 op_sel_hi:[0,0,0] cbsz:4 blgp:2
	v_mfma_scale_f32_16x16x128_f8f6f4 v[44:47], v[136:139], v[202:207], v[44:47], v210, v219 op_sel_hi:[0,0,0] cbsz:4 blgp:2
	v_mfma_scale_f32_16x16x128_f8f6f4 v[48:51], v[140:143], v[184:189], v[48:51], v211, v216 op_sel_hi:[0,0,0] cbsz:4 blgp:2
	v_mfma_scale_f32_16x16x128_f8f6f4 v[52:55], v[140:143], v[190:195], v[52:55], v211, v217 op_sel_hi:[0,0,0] cbsz:4 blgp:2
	s_add_u32 m0, s40, 0x2000
	ds_read_b128 v[136:139], v240 offset:2048
	ds_read_b128 v[172:175], v241 offset:3072
	ds_read_b64 v[176:177], v242 offset:3072
	buffer_load_dwordx4 v225, s[4:7], s36 offen lds
	v_mfma_scale_f32_16x16x128_f8f6f4 v[56:59], v[140:143], v[196:201], v[56:59], v211, v218 op_sel_hi:[0,0,0] cbsz:4 blgp:2
	v_mfma_scale_f32_16x16x128_f8f6f4 v[60:63], v[140:143], v[202:207], v[60:63], v211, v219 op_sel_hi:[0,0,0] cbsz:4 blgp:2
	v_mfma_scale_f32_16x16x128_f8f6f4 v[64:67], v[144:147], v[184:189], v[64:67], v212, v216 op_sel_hi:[0,0,0] cbsz:4 blgp:2
	v_mfma_scale_f32_16x16x128_f8f6f4 v[68:71], v[144:147], v[190:195], v[68:71], v212, v217 op_sel_hi:[0,0,0] cbsz:4 blgp:2
	s_add_u32 m0, s40, 0x4000
	ds_read_b128 v[140:143], v240 offset:3072
	ds_read_b128 v[178:181], v241 offset:4608
	ds_read_b64 v[182:183], v242 offset:4608
	buffer_load_dwordx4 v221, s[4:7], s37 offen lds
	v_mfma_scale_f32_16x16x128_f8f6f4 v[72:75], v[144:147], v[196:201], v[72:75], v212, v218 op_sel_hi:[0,0,0] cbsz:4 blgp:2
	v_mfma_scale_f32_16x16x128_f8f6f4 v[76:79], v[144:147], v[202:207], v[76:79], v212, v219 op_sel_hi:[0,0,0] cbsz:4 blgp:2
	v_mfma_scale_f32_16x16x128_f8f6f4 v[80:83], v[148:151], v[184:189], v[80:83], v213, v216 op_sel_hi:[0,0,0] cbsz:4 blgp:2
	v_mfma_scale_f32_16x16x128_f8f6f4 v[84:87], v[148:151], v[190:195], v[84:87], v213, v217 op_sel_hi:[0,0,0] cbsz:4 blgp:2
	s_add_u32 m0, s40, 0x6000
	ds_read_b128 v[144:147], v240 offset:4096
	buffer_load_dwordx4 v225, s[4:7], s37 offen lds
	v_mfma_scale_f32_16x16x128_f8f6f4 v[88:91], v[148:151], v[196:201], v[88:91], v213, v218 op_sel_hi:[0,0,0] cbsz:4 blgp:2
	v_mfma_scale_f32_16x16x128_f8f6f4 v[92:95], v[148:151], v[202:207], v[92:95], v213, v219 op_sel_hi:[0,0,0] cbsz:4 blgp:2
	v_mfma_scale_f32_16x16x128_f8f6f4 v[96:99], v[244:247], v[184:189], v[96:99], v214, v216 op_sel_hi:[0,0,0] cbsz:4 blgp:2
	v_mfma_scale_f32_16x16x128_f8f6f4 v[100:103], v[244:247], v[190:195], v[100:103], v214, v217 op_sel_hi:[0,0,0] cbsz:4 blgp:2
	s_add_u32 m0, s40, 0x8000
	ds_read_b128 v[148:151], v240 offset:5120
	buffer_load_dwordx4 v226, s[4:7], s37 offen lds
	s_add_u32 s36, s36, 0x4000
	s_add_u32 s37, s37, 0x6000
	s_add_u32 s40, s40, 0xa000
	s_sub_u32 s41, s40, 0x1e000
	s_cmp_ge_u32 s40, s49
	s_cselect_b32 s40, s41, s40
	v_mfma_scale_f32_16x16x128_f8f6f4 v[104:107], v[244:247], v[196:201], v[104:107], v214, v218 op_sel_hi:[0,0,0] cbsz:4 blgp:2
	v_mfma_scale_f32_16x16x128_f8f6f4 v[108:111], v[244:247], v[202:207], v[108:111], v214, v219 op_sel_hi:[0,0,0] cbsz:4 blgp:2
	v_mfma_scale_f32_16x16x128_f8f6f4 v[112:115], v[252:255], v[184:189], v[112:115], v215, v216 op_sel_hi:[0,0,0] cbsz:4 blgp:2
	v_mfma_scale_f32_16x16x128_f8f6f4 v[116:119], v[252:255], v[190:195], v[116:119], v215, v217 op_sel_hi:[0,0,0] cbsz:4 blgp:2
	v_mfma_scale_f32_16x16x128_f8f6f4 v[120:123], v[252:255], v[196:201], v[120:123], v215, v218 op_sel_hi:[0,0,0] cbsz:4 blgp:2
	v_mfma_scale_f32_16x16x128_f8f6f4 v[124:127], v[252:255], v[202:207], v[124:127], v215, v219 op_sel_hi:[0,0,0] cbsz:4 blgp:2
	s_add_u32 s34, s34, 1
.Lkloop1:
	s_waitcnt vmcnt(5)
	s_waitcnt lgkmcnt(0)
	s_barrier
	s_mul_i32 s35, s33, 0xa000
	v_add_u32_e32 v240, s35, v222
	v_add_u32_e32 v241, s35, v223
	v_add_u32_e32 v242, s35, v224
	s_add_u32 s33, s33, 1
	s_cmp_eq_u32 s33, 3
	s_cselect_b32 s33, 0, s33
	ds_read_b128 v[244:247], v240 offset:6144
	ds_read_b128 v[252:255], v240 offset:7168
	v_mfma_scale_f32_16x16x128_f8f6f4 v[0:3], v[128:131], v[160:165], v[0:3], v208, v216 op_sel_hi:[0,0,0] cbsz:4 blgp:2
	v_mfma_scale_f32_16x16x128_f8f6f4 v[4:7], v[128:131], v[166:171], v[4:7], v208, v217 op_sel_hi:[0,0,0] cbsz:4 blgp:2
	v_mfma_scale_f32_16x16x128_f8f6f4 v[8:11], v[128:131], v[172:177], v[8:11], v208, v218 op_sel_hi:[0,0,0] cbsz:4 blgp:2
	v_mfma_scale_f32_16x16x128_f8f6f4 v[12:15], v[128:131], v[178:183], v[12:15], v208, v219 op_sel_hi:[0,0,0] cbsz:4 blgp:2
	v_mfma_scale_f32_16x16x128_f8f6f4 v[16:19], v[132:135], v[160:165], v[16:19], v209, v216 op_sel_hi:[0,0,0] cbsz:4 blgp:2
	v_mfma_scale_f32_16x16x128_f8f6f4 v[20:23], v[132:135], v[166:171], v[20:23], v209, v217 op_sel_hi:[0,0,0] cbsz:4 blgp:2
	ds_read_b128 v[128:131], v240 offset:0
	ds_read_b128 v[184:187], v241 offset:0
	ds_read_b64 v[188:189], v242 offset:0
	v_mfma_scale_f32_16x16x128_f8f6f4 v[24:27], v[132:135], v[172:177], v[24:27], v209, v218 op_sel_hi:[0,0,0] cbsz:4 blgp:2
	v_mfma_scale_f32_16x16x128_f8f6f4 v[28:31], v[132:135], v[178:183], v[28:31], v209, v219 op_sel_hi:[0,0,0] cbsz:4 blgp:2
	v_mfma_scale_f32_16x16x128_f8f6f4 v[32:35], v[136:139], v[160:165], v[32:35], v210, v216 op_sel_hi:[0,0,0] cbsz:4 blgp:2
	v_mfma_scale_f32_16x16x128_f8f6f4 v[36:39], v[136:139], v[166:171], v[36:39], v210, v217 op_sel_hi:[0,0,0] cbsz:4 blgp:2
	s_cmp_eq_u32 s34, 13
	s_cselect_b32 s36, s38, s36
	s_cselect_b32 s37, s39, s37
	s_mov_b32 m0, s40
	ds_read_b128 v[132:135], v240 offset:1024
	ds_read_b128 v[190:193], v241 offset:1536
	ds_read_b64 v[194:195], v242 offset:1536
	buffer_load_dwordx4 v221, s[4:7], s36 offen lds
	v_mfma_scale_f32_16x16x128_f8f6f4 v[40:43], v[136:139], v[172:177], v[40:43], v210, v218 op_sel_hi:[0,0,0] cbsz:4 blgp:2
	v_mfma_scale_f32_16x16x128_f8f6f4 v[44:47], v[136:139], v[178:183], v[44:47], v210, v219 op_sel_hi:[0,0,0] cbsz:4 blgp:2
	v_mfma_scale_f32_16x16x128_f8f6f4 v[48:51], v[140:143], v[160:165], v[48:51], v211, v216 op_sel_hi:[0,0,0] cbsz:4 blgp:2
	v_mfma_scale_f32_16x16x128_f8f6f4 v[52:55], v[140:143], v[166:171], v[52:55], v211, v217 op_sel_hi:[0,0,0] cbsz:4 blgp:2
	s_add_u32 m0, s40, 0x2000
	ds_read_b128 v[136:139], v240 offset:2048
	ds_read_b128 v[196:199], v241 offset:3072
	ds_read_b64 v[200:201], v242 offset:3072
	buffer_load_dwordx4 v225, s[4:7], s36 offen lds
	v_mfma_scale_f32_16x16x128_f8f6f4 v[56:59], v[140:143], v[172:177], v[56:59], v211, v218 op_sel_hi:[0,0,0] cbsz:4 blgp:2
	v_mfma_scale_f32_16x16x128_f8f6f4 v[60:63], v[140:143], v[178:183], v[60:63], v211, v219 op_sel_hi:[0,0,0] cbsz:4 blgp:2
	v_mfma_scale_f32_16x16x128_f8f6f4 v[64:67], v[144:147], v[160:165], v[64:67], v212, v216 op_sel_hi:[0,0,0] cbsz:4 blgp:2
	v_mfma_scale_f32_16x16x128_f8f6f4 v[68:71], v[144:147], v[166:171], v[68:71], v212, v217 op_sel_hi:[0,0,0] cbsz:4 blgp:2
	s_add_u32 m0, s40, 0x4000
	ds_read_b128 v[140:143], v240 offset:3072
	ds_read_b128 v[202:205], v241 offset:4608
	ds_read_b64 v[206:207], v242 offset:4608
	buffer_load_dwordx4 v221, s[4:7], s37 offen lds
	v_mfma_scale_f32_16x16x128_f8f6f4 v[72:75], v[144:147], v[172:177], v[72:75], v212, v218 op_sel_hi:[0,0,0] cbsz:4 blgp:2
	v_mfma_scale_f32_16x16x128_f8f6f4 v[76:79], v[144:147], v[178:183], v[76:79], v212, v219 op_sel_hi:[0,0,0] cbsz:4 blgp:2
	v_mfma_scale_f32_16x16x128_f8f6f4 v[80:83], v[148:151], v[160:165], v[80:83], v213, v216 op_sel_hi:[0,0,0] cbsz:4 blgp:2
	v_mfma_scale_f32_16x16x128_f8f6f4 v[84:87], v[148:151], v[166:171], v[84:87], v213, v217 op_sel_hi:[0,0,0] cbsz:4 blgp:2
	s_add_u32 m0, s40, 0x6000
	ds_read_b128 v[144:147], v240 offset:4096
	buffer_load_dwordx4 v225, s[4:7], s37 offen lds
	v_mfma_scale_f32_16x16x128_f8f6f4 v[88:91], v[148:151], v[172:177], v[88:91], v213, v218 op_sel_hi:[0,0,0] cbsz:4 blgp:2
	v_mfma_scale_f32_16x16x128_f8f6f4 v[92:95], v[148:151], v[178:183], v[92:95], v213, v219 op_sel_hi:[0,0,0] cbsz:4 blgp:2
	v_mfma_scale_f32_16x16x128_f8f6f4 v[96:99], v[152:155], v[160:165], v[96:99], v214, v216 op_sel_hi:[0,0,0] cbsz:4 blgp:2
	v_mfma_scale_f32_16x16x128_f8f6f4 v[100:103], v[152:155], v[166:171], v[100:103], v214, v217 op_sel_hi:[0,0,0] cbsz:4 blgp:2
	s_add_u32 m0, s40, 0x8000
	ds_read_b128 v[148:151], v240 offset:5120
	buffer_load_dwordx4 v226, s[4:7], s37 offen lds
	s_add_u32 s36, s36, 0x4000
	s_add_u32 s37, s37, 0x6000
	s_add_u32 s40, s40, 0xa000
	s_sub_u32 s41, s40, 0x1e000
	s_cmp_ge_u32 s40, s49
	s_cselect_b32 s40, s41, s40
	v_mfma_scale_f32_16x16x128_f8f6f4 v[104:107], v[152:155], v[172:177], v[104:107], v214, v218 op_sel_hi:[0,0,0] cbsz:4 blgp:2
	v_mfma_scale_f32_16x16x128_f8f6f4 v[108:111], v[152:155], v[178:183], v[108:111], v214, v219 op_sel_hi:[0,0,0] cbsz:4 blgp:2
	v_mfma_scale_f32_16x16x128_f8f6f4 v[112:115], v[156:159], v[160:165], v[112:115], v215, v216 op_sel_hi:[0,0,0] cbsz:4 blgp:2
	v_mfma_scale_f32_16x16x128_f8f6f4 v[116:119], v[156:159], v[166:171], v[116:119], v215, v217 op_sel_hi:[0,0,0] cbsz:4 blgp:2
	v_mfma_scale_f32_16x16x128_f8f6f4 v[120:123], v[156:159], v[172:177], v[120:123], v215, v218 op_sel_hi:[0,0,0] cbsz:4 blgp:2
	v_mfma_scale_f32_16x16x128_f8f6f4 v[124:127], v[156:159], v[178:183], v[124:127], v215, v219 op_sel_hi:[0,0,0] cbsz:4 blgp:2
	s_add_u32 s34, s34, 1
	s_waitcnt vmcnt(5)
	s_waitcnt lgkmcnt(0)
	s_barrier
	s_mul_i32 s35, s33, 0xa000
	v_add_u32_e32 v240, s35, v222
	v_add_u32_e32 v241, s35, v223
	v_add_u32_e32 v242, s35, v224
	s_add_u32 s33, s33, 1
	s_cmp_eq_u32 s33, 3
	s_cselect_b32 s33, 0, s33
	ds_read_b128 v[152:155], v240 offset:6144
	ds_read_b128 v[156:159], v240 offset:7168
	v_mfma_scale_f32_16x16x128_f8f6f4 v[0:3], v[128:131], v[184:189], v[0:3], v208, v216 op_sel_hi:[0,0,0] cbsz:4 blgp:2
	v_mfma_scale_f32_16x16x128_f8f6f4 v[4:7], v[128:131], v[190:195], v[4:7], v208, v217 op_sel_hi:[0,0,0] cbsz:4 blgp:2
	v_mfma_scale_f32_16x16x128_f8f6f4 v[8:11], v[128:131], v[196:201], v[8:11], v208, v218 op_sel_hi:[0,0,0] cbsz:4 blgp:2
	v_mfma_scale_f32_16x16x128_f8f6f4 v[12:15], v[128:131], v[202:207], v[12:15], v208, v219 op_sel_hi:[0,0,0] cbsz:4 blgp:2
	v_mfma_scale_f32_16x16x128_f8f6f4 v[16:19], v[132:135], v[184:189], v[16:19], v209, v216 op_sel_hi:[0,0,0] cbsz:4 blgp:2
	v_mfma_scale_f32_16x16x128_f8f6f4 v[20:23], v[132:135], v[190:195], v[20:23], v209, v217 op_sel_hi:[0,0,0] cbsz:4 blgp:2
	ds_read_b128 v[128:131], v240 offset:0
	ds_read_b128 v[160:163], v241 offset:0
	ds_read_b64 v[164:165], v242 offset:0
	v_mfma_scale_f32_16x16x128_f8f6f4 v[24:27], v[132:135], v[196:201], v[24:27], v209, v218 op_sel_hi:[0,0,0] cbsz:4 blgp:2
	v_mfma_scale_f32_16x16x128_f8f6f4 v[28:31], v[132:135], v[202:207], v[28:31], v209, v219 op_sel_hi:[0,0,0] cbsz:4 blgp:2
	v_mfma_scale_f32_16x16x128_f8f6f4 v[32:35], v[136:139], v[184:189], v[32:35], v210, v216 op_sel_hi:[0,0,0] cbsz:4 blgp:2
	v_mfma_scale_f32_16x16x128_f8f6f4 v[36:39], v[136:139], v[190:195], v[36:39], v210, v217 op_sel_hi:[0,0,0] cbsz:4 blgp:2
	s_cmp_eq_u32 s34, 13
	s_cselect_b32 s36, s38, s36
	s_cselect_b32 s37, s39, s37
	s_mov_b32 m0, s40
	ds_read_b128 v[132:135], v240 offset:1024
	ds_read_b128 v[166:169], v241 offset:1536
	ds_read_b64 v[170:171], v242 offset:1536
	buffer_load_dwordx4 v221, s[4:7], s36 offen lds
	v_mfma_scale_f32_16x16x128_f8f6f4 v[40:43], v[136:139], v[196:201], v[40:43], v210, v218 op_sel_hi:[0,0,0] cbsz:4 blgp:2
	v_mfma_scale_f32_16x16x128_f8f6f4 v[44:47], v[136:139], v[202:207], v[44:47], v210, v219 op_sel_hi:[0,0,0] cbsz:4 blgp:2
	v_mfma_scale_f32_16x16x128_f8f6f4 v[48:51], v[140:143], v[184:189], v[48:51], v211, v216 op_sel_hi:[0,0,0] cbsz:4 blgp:2
	v_mfma_scale_f32_16x16x128_f8f6f4 v[52:55], v[140:143], v[190:195], v[52:55], v211, v217 op_sel_hi:[0,0,0] cbsz:4 blgp:2
	s_add_u32 m0, s40, 0x2000
	ds_read_b128 v[136:139], v240 offset:2048
	ds_read_b128 v[172:175], v241 offset:3072
	ds_read_b64 v[176:177], v242 offset:3072
	buffer_load_dwordx4 v225, s[4:7], s36 offen lds
	v_mfma_scale_f32_16x16x128_f8f6f4 v[56:59], v[140:143], v[196:201], v[56:59], v211, v218 op_sel_hi:[0,0,0] cbsz:4 blgp:2
	v_mfma_scale_f32_16x16x128_f8f6f4 v[60:63], v[140:143], v[202:207], v[60:63], v211, v219 op_sel_hi:[0,0,0] cbsz:4 blgp:2
	v_mfma_scale_f32_16x16x128_f8f6f4 v[64:67], v[144:147], v[184:189], v[64:67], v212, v216 op_sel_hi:[0,0,0] cbsz:4 blgp:2
	v_mfma_scale_f32_16x16x128_f8f6f4 v[68:71], v[144:147], v[190:195], v[68:71], v212, v217 op_sel_hi:[0,0,0] cbsz:4 blgp:2
	s_add_u32 m0, s40, 0x4000
	ds_read_b128 v[140:143], v240 offset:3072
	ds_read_b128 v[178:181], v241 offset:4608
	ds_read_b64 v[182:183], v242 offset:4608
	buffer_load_dwordx4 v221, s[4:7], s37 offen lds
	v_mfma_scale_f32_16x16x128_f8f6f4 v[72:75], v[144:147], v[196:201], v[72:75], v212, v218 op_sel_hi:[0,0,0] cbsz:4 blgp:2
	v_mfma_scale_f32_16x16x128_f8f6f4 v[76:79], v[144:147], v[202:207], v[76:79], v212, v219 op_sel_hi:[0,0,0] cbsz:4 blgp:2
	v_mfma_scale_f32_16x16x128_f8f6f4 v[80:83], v[148:151], v[184:189], v[80:83], v213, v216 op_sel_hi:[0,0,0] cbsz:4 blgp:2
	v_mfma_scale_f32_16x16x128_f8f6f4 v[84:87], v[148:151], v[190:195], v[84:87], v213, v217 op_sel_hi:[0,0,0] cbsz:4 blgp:2
	s_add_u32 m0, s40, 0x6000
	ds_read_b128 v[144:147], v240 offset:4096
	buffer_load_dwordx4 v225, s[4:7], s37 offen lds
	v_mfma_scale_f32_16x16x128_f8f6f4 v[88:91], v[148:151], v[196:201], v[88:91], v213, v218 op_sel_hi:[0,0,0] cbsz:4 blgp:2
	v_mfma_scale_f32_16x16x128_f8f6f4 v[92:95], v[148:151], v[202:207], v[92:95], v213, v219 op_sel_hi:[0,0,0] cbsz:4 blgp:2
	v_mfma_scale_f32_16x16x128_f8f6f4 v[96:99], v[244:247], v[184:189], v[96:99], v214, v216 op_sel_hi:[0,0,0] cbsz:4 blgp:2
	v_mfma_scale_f32_16x16x128_f8f6f4 v[100:103], v[244:247], v[190:195], v[100:103], v214, v217 op_sel_hi:[0,0,0] cbsz:4 blgp:2
	s_add_u32 m0, s40, 0x8000
	ds_read_b128 v[148:151], v240 offset:5120
	buffer_load_dwordx4 v226, s[4:7], s37 offen lds
	s_add_u32 s36, s36, 0x4000
	s_add_u32 s37, s37, 0x6000
	s_add_u32 s40, s40, 0xa000
	s_sub_u32 s41, s40, 0x1e000
	s_cmp_ge_u32 s40, s49
	s_cselect_b32 s40, s41, s40
	v_mfma_scale_f32_16x16x128_f8f6f4 v[104:107], v[244:247], v[196:201], v[104:107], v214, v218 op_sel_hi:[0,0,0] cbsz:4 blgp:2
	v_mfma_scale_f32_16x16x128_f8f6f4 v[108:111], v[244:247], v[202:207], v[108:111], v214, v219 op_sel_hi:[0,0,0] cbsz:4 blgp:2
	v_mfma_scale_f32_16x16x128_f8f6f4 v[112:115], v[252:255], v[184:189], v[112:115], v215, v216 op_sel_hi:[0,0,0] cbsz:4 blgp:2
	v_mfma_scale_f32_16x16x128_f8f6f4 v[116:119], v[252:255], v[190:195], v[116:119], v215, v217 op_sel_hi:[0,0,0] cbsz:4 blgp:2
	s_cmp_eq_u32 s34, 13
	s_cbranch_scc0 .Lnosc_or1
	s_add_u32 s44, s23, 1
	s_and_b32 s44, s44, 1
	s_cmp_lt_u32 s18, 4
	s_cselect_b32 s80, s26, s27
	s_cselect_b32 s82, s8, s10
	s_cselect_b32 s83, s9, s11
	s_lshl_b32 s80, s80, 10
	s_and_b32 s84, s18, 3
	s_lshl_b32 s84, s84, 8
	s_add_u32 s80, s80, s84
	s_add_u32 s82, s82, s80
	s_addc_u32 s83, s83, 0
	s_lshl_b32 s84, s44, 11
	s_lshl_b32 s85, s18, 8
	s_add_u32 s84, s84, s85
	s_add_u32 s84, s84, 0x1e000
	s_mov_b32 m0, s84
	v_lshlrev_b32_e32 v236, 2, v220
	global_load_lds_dword v236, s[82:83]
.Lnosc_or1:
	v_mfma_scale_f32_16x16x128_f8f6f4 v[120:123], v[252:255], v[196:201], v[120:123], v215, v218 op_sel_hi:[0,0,0] cbsz:4 blgp:2
	v_mfma_scale_f32_16x16x128_f8f6f4 v[124:127], v[252:255], v[202:207], v[124:127], v215, v219 op_sel_hi:[0,0,0] cbsz:4 blgp:2
	s_add_u32 s34, s34, 1
	s_cmp_lt_u32 s34, 16
	s_cbranch_scc1 .Lkloop1
	s_add_u32 s44, s23, 1
	s_and_b32 s44, s44, 1
	s_lshl_b32 s80, s44, 11
	s_add_u32 s80, s80, 0x1e000
	s_lshl_b32 s82, s19, 9
	s_add_u32 s82, s82, s80
	s_lshl_b32 s83, s20, 8
	s_add_u32 s83, s83, s80
	s_add_u32 s83, s83, 0x400
	v_and_b32_e32 v234, 15, v220
	v_lshlrev_b32_e32 v234, 2, v234
	v_add_u32_e32 v235, s83, v234
	v_add_u32_e32 v234, s82, v234
	ds_read_b32 v208, v234 offset:0
	ds_read_b32 v209, v234 offset:64
	ds_read_b32 v210, v234 offset:128
	ds_read_b32 v211, v234 offset:192
	ds_read_b32 v212, v234 offset:256
	ds_read_b32 v213, v234 offset:320
	ds_read_b32 v214, v234 offset:384
	ds_read_b32 v215, v234 offset:448
	ds_read_b32 v216, v235 offset:0
	ds_read_b32 v217, v235 offset:64
	ds_read_b32 v218, v235 offset:128
	ds_read_b32 v219, v235 offset:192
	v_exp_f32_e32 v236, v0
	v_exp_f32_e32 v237, v1
	v_exp_f32_e32 v238, v2
	v_exp_f32_e32 v239, v3
	s_add_u32 s23, s23, 1
	v_exp_f32_e32 v240, v16
	v_exp_f32_e32 v241, v17
	v_exp_f32_e32 v242, v18
	v_exp_f32_e32 v243, v19
	s_mov_b32 s24, s26
	v_mov_b32_e32 v228, v236
	v_mov_b32_e32 v229, v237
	v_pk_add_f32 v[228:229], v[228:229], v[238:239]
	v_pk_add_f32 v[228:229], v[228:229], v[240:241]
	s_mov_b32 s25, s27
	v_pk_add_f32 v[228:229], v[228:229], v[242:243]
	v_exp_f32_e32 v236, v32
	v_exp_f32_e32 v237, v33
	v_exp_f32_e32 v238, v34
	s_mov_b32 s28, s30
	v_exp_f32_e32 v239, v35
	v_exp_f32_e32 v240, v48
	v_exp_f32_e32 v241, v49
	v_exp_f32_e32 v242, v50
	s_mov_b32 s29, s31
	v_exp_f32_e32 v243, v51
	v_pk_add_f32 v[228:229], v[228:229], v[236:237]
	v_pk_add_f32 v[228:229], v[228:229], v[238:239]
	v_pk_add_f32 v[228:229], v[228:229], v[240:241]
	s_add_u32 s45, s23, 1
	v_pk_add_f32 v[228:229], v[228:229], v[242:243]
	v_exp_f32_e32 v236, v64
	v_exp_f32_e32 v237, v65
	v_exp_f32_e32 v238, v66
	s_sub_u32 s46, s22, 1
	v_exp_f32_e32 v239, v67
	v_exp_f32_e32 v240, v80
	v_exp_f32_e32 v241, v81
	v_exp_f32_e32 v242, v82
	s_min_u32 s45, s45, s46
	v_exp_f32_e32 v243, v83
	v_pk_add_f32 v[228:229], v[228:229], v[236:237]
	v_pk_add_f32 v[228:229], v[228:229], v[238:239]
	v_pk_add_f32 v[228:229], v[228:229], v[240:241]
	s_lshl_b32 s45, s45, 5
	v_pk_add_f32 v[228:229], v[228:229], v[242:243]
	v_exp_f32_e32 v236, v96
	v_exp_f32_e32 v237, v97
	v_exp_f32_e32 v238, v98
	s_add_u32 s45, s45, s21
	v_exp_f32_e32 v239, v99
	v_exp_f32_e32 v240, v112
	v_exp_f32_e32 v241, v113
	v_exp_f32_e32 v242, v114
	s_lshr_b32 s80, s45, 5
	v_exp_f32_e32 v243, v115
	v_pk_add_f32 v[228:229], v[228:229], v[236:237]
	v_pk_add_f32 v[228:229], v[228:229], v[238:239]
	v_pk_add_f32 v[228:229], v[228:229], v[240:241]
	s_and_b32 s82, s45, 31
	v_pk_add_f32 v[228:229], v[228:229], v[242:243]
	v_exp_f32_e32 v236, v4
	v_exp_f32_e32 v237, v5
	v_exp_f32_e32 v238, v6
	s_lshr_b32 s83, s80, 1
	v_exp_f32_e32 v239, v7
	v_exp_f32_e32 v240, v20
	v_exp_f32_e32 v241, v21
	v_exp_f32_e32 v242, v22
	s_lshl_b32 s83, s83, 2
	v_exp_f32_e32 v243, v23
	v_mov_b32_e32 v230, v236
	v_mov_b32_e32 v231, v237
	v_pk_add_f32 v[230:231], v[230:231], v[238:239]
	s_lshr_b32 s84, s82, 3
	v_pk_add_f32 v[230:231], v[230:231], v[240:241]
	v_pk_add_f32 v[230:231], v[230:231], v[242:243]
	v_exp_f32_e32 v236, v36
	v_exp_f32_e32 v237, v37
	s_add_u32 s83, s83, s84
	v_exp_f32_e32 v238, v38
	v_exp_f32_e32 v239, v39
	v_exp_f32_e32 v240, v52
	v_exp_f32_e32 v241, v53
	s_and_b32 s84, s80, 1
	v_exp_f32_e32 v242, v54
	v_exp_f32_e32 v243, v55
	v_pk_add_f32 v[230:231], v[230:231], v[236:237]
	v_pk_add_f32 v[230:231], v[230:231], v[238:239]
	s_lshl_b32 s84, s84, 3
	v_pk_add_f32 v[230:231], v[230:231], v[240:241]
	v_pk_add_f32 v[230:231], v[230:231], v[242:243]
	v_exp_f32_e32 v236, v68
	v_exp_f32_e32 v237, v69
	s_and_b32 s85, s82, 7
	v_exp_f32_e32 v238, v70
	v_exp_f32_e32 v239, v71
	v_exp_f32_e32 v240, v84
	v_exp_f32_e32 v241, v85
	s_add_u32 s84, s84, s85
	v_exp_f32_e32 v242, v86
	v_exp_f32_e32 v243, v87
	v_pk_add_f32 v[230:231], v[230:231], v[236:237]
	v_pk_add_f32 v[230:231], v[230:231], v[238:239]
	s_sub_u32 s85, s45, 0x7c0
	v_pk_add_f32 v[230:231], v[230:231], v[240:241]
	v_pk_add_f32 v[230:231], v[230:231], v[242:243]
	v_exp_f32_e32 v236, v100
	v_exp_f32_e32 v237, v101
	s_cmpk_gt_u32 s45, 0x7bf
	v_exp_f32_e32 v238, v102
	v_exp_f32_e32 v239, v103
	v_exp_f32_e32 v240, v116
	v_exp_f32_e32 v241, v117
	s_cselect_b32 s26, 0x7c, s83
	v_exp_f32_e32 v242, v118
	v_exp_f32_e32 v243, v119
	v_pk_add_f32 v[230:231], v[230:231], v[236:237]
	v_pk_add_f32 v[230:231], v[230:231], v[238:239]
	s_cselect_b32 s27, s85, s84
	v_pk_add_f32 v[230:231], v[230:231], v[240:241]
	v_pk_add_f32 v[230:231], v[230:231], v[242:243]
	v_exp_f32_e32 v236, v8
	v_exp_f32_e32 v237, v9
	s_lshl_b32 s30, s26, 18
	v_exp_f32_e32 v238, v10
	v_exp_f32_e32 v239, v11
	v_exp_f32_e32 v240, v24
	v_exp_f32_e32 v241, v25
	s_mul_i32 s31, s27, 0x60000
	v_exp_f32_e32 v242, v26
	v_exp_f32_e32 v243, v27
	v_mov_b32_e32 v232, v236
	v_mov_b32_e32 v233, v237
	s_add_u32 s31, s31, 0x1f40000
	v_pk_add_f32 v[232:233], v[232:233], v[238:239]
	v_pk_add_f32 v[232:233], v[232:233], v[240:241]
	v_pk_add_f32 v[232:233], v[232:233], v[242:243]
	v_exp_f32_e32 v236, v40
	s_add_u32 s38, s30, s48
	v_exp_f32_e32 v237, v41
	v_exp_f32_e32 v238, v42
	v_exp_f32_e32 v239, v43
	v_exp_f32_e32 v240, v56
	s_add_u32 s39, s31, s48
	v_exp_f32_e32 v241, v57
	v_exp_f32_e32 v242, v58
	v_exp_f32_e32 v243, v59
	v_pk_add_f32 v[232:233], v[232:233], v[236:237]
	v_pk_add_f32 v[232:233], v[232:233], v[238:239]
	v_pk_add_f32 v[232:233], v[232:233], v[240:241]
	v_pk_add_f32 v[232:233], v[232:233], v[242:243]
	v_exp_f32_e32 v236, v72
	v_exp_f32_e32 v237, v73
	v_exp_f32_e32 v238, v74
	v_exp_f32_e32 v239, v75
	v_exp_f32_e32 v240, v88
	v_exp_f32_e32 v241, v89
	v_exp_f32_e32 v242, v90
	v_exp_f32_e32 v243, v91
	v_pk_add_f32 v[232:233], v[232:233], v[236:237]
	v_pk_add_f32 v[232:233], v[232:233], v[238:239]
	v_pk_add_f32 v[232:233], v[232:233], v[240:241]
	v_pk_add_f32 v[232:233], v[232:233], v[242:243]
	v_exp_f32_e32 v236, v104
	v_exp_f32_e32 v237, v105
	v_exp_f32_e32 v238, v106
	v_exp_f32_e32 v239, v107
	v_exp_f32_e32 v240, v120
	v_exp_f32_e32 v241, v121
	v_exp_f32_e32 v242, v122
	v_exp_f32_e32 v243, v123
	v_pk_add_f32 v[232:233], v[232:233], v[236:237]
	v_pk_add_f32 v[232:233], v[232:233], v[238:239]
	v_pk_add_f32 v[232:233], v[232:233], v[240:241]
	v_pk_add_f32 v[232:233], v[232:233], v[242:243]
	v_exp_f32_e32 v236, v12
	v_exp_f32_e32 v237, v13
	v_exp_f32_e32 v238, v14
	v_exp_f32_e32 v239, v15
	v_exp_f32_e32 v240, v28
	v_exp_f32_e32 v241, v29
	v_exp_f32_e32 v242, v30
	v_exp_f32_e32 v243, v31
	v_mov_b32_e32 v234, v236
	v_mov_b32_e32 v235, v237
	v_pk_add_f32 v[234:235], v[234:235], v[238:239]
	v_pk_add_f32 v[234:235], v[234:235], v[240:241]
	v_pk_add_f32 v[234:235], v[234:235], v[242:243]
	v_exp_f32_e32 v236, v44
	v_exp_f32_e32 v237, v45
	v_exp_f32_e32 v238, v46
	v_exp_f32_e32 v239, v47
	v_exp_f32_e32 v240, v60
	v_exp_f32_e32 v241, v61
	v_exp_f32_e32 v242, v62
	v_exp_f32_e32 v243, v63
	v_pk_add_f32 v[234:235], v[234:235], v[236:237]
	v_pk_add_f32 v[234:235], v[234:235], v[238:239]
	v_pk_add_f32 v[234:235], v[234:235], v[240:241]
	v_pk_add_f32 v[234:235], v[234:235], v[242:243]
	v_exp_f32_e32 v236, v76
	v_exp_f32_e32 v237, v77
	v_exp_f32_e32 v238, v78
	v_exp_f32_e32 v239, v79
	v_exp_f32_e32 v240, v92
	v_exp_f32_e32 v241, v93
	v_exp_f32_e32 v242, v94
	v_exp_f32_e32 v243, v95
	v_pk_add_f32 v[234:235], v[234:235], v[236:237]
	v_pk_add_f32 v[234:235], v[234:235], v[238:239]
	v_pk_add_f32 v[234:235], v[234:235], v[240:241]
	v_pk_add_f32 v[234:235], v[234:235], v[242:243]
	v_exp_f32_e32 v236, v108
	v_exp_f32_e32 v237, v109
	v_exp_f32_e32 v238, v110
	v_exp_f32_e32 v239, v111
	v_exp_f32_e32 v240, v124
	v_exp_f32_e32 v241, v125
	v_exp_f32_e32 v242, v126
	v_exp_f32_e32 v243, v127
	v_pk_add_f32 v[234:235], v[234:235], v[236:237]
	v_pk_add_f32 v[234:235], v[234:235], v[238:239]
	v_pk_add_f32 v[234:235], v[234:235], v[240:241]
	v_pk_add_f32 v[234:235], v[234:235], v[242:243]
	v_add_f32_e32 v228, v228, v229
	v_add_f32_e32 v230, v230, v231
	v_add_f32_e32 v232, v232, v233
	v_add_f32_e32 v234, v234, v235
	v_mov_b32_e32 v229, v228
	v_mov_b32_e32 v231, v230
	v_mov_b32_e32 v233, v232
	v_mov_b32_e32 v235, v234
	s_nop 1
	v_permlane16_swap_b32_e32 v228, v229
	v_permlane16_swap_b32_e32 v230, v231
	v_permlane16_swap_b32_e32 v232, v233
	v_permlane16_swap_b32_e32 v234, v235
	s_nop 1
	v_add_f32_e32 v228, v228, v229
	v_add_f32_e32 v230, v230, v231
	v_add_f32_e32 v232, v232, v233
	v_add_f32_e32 v234, v234, v235
	v_mov_b32_e32 v229, v228
	v_mov_b32_e32 v231, v230
	v_mov_b32_e32 v233, v232
	v_mov_b32_e32 v235, v234
	s_nop 1
	v_permlane32_swap_b32_e32 v228, v229
	v_permlane32_swap_b32_e32 v230, v231
	v_permlane32_swap_b32_e32 v232, v233
	v_permlane32_swap_b32_e32 v234, v235
	s_nop 1
	v_add_f32_e32 v228, v228, v229
	v_add_f32_e32 v230, v230, v231
	v_add_f32_e32 v232, v232, v233
	v_add_f32_e32 v234, v234, v235
	v_mov_b32_e32 v238, v228
	v_cndmask_b32_e64 v238, v238, v230, s[50:51]
	v_cndmask_b32_e64 v238, v238, v232, s[52:53]
	v_cndmask_b32_e64 v238, v238, v234, s[54:55]
	v_cmp_nle_f32_e64 s[60:61], s56, v238
	v_cmp_nge_f32_e64 s[58:59], s57, v238
	s_nop 3
	s_or_b64 s[58:59], s[58:59], s[60:61]
	s_cmp_lg_u64 s[58:59], 0
	s_cbranch_scc1 .Lslow1
	global_atomic_add_f32 v[248:249], v238, off
	s_branch .Lepi_done1

	.amdhsa_kernel _Z15gemm_lse_kernelPKhS0_PKjS2_PfPiP15HIP_vector_typeIfLj2EE
		.amdhsa_group_segment_fixed_size 126976
		.amdhsa_private_segment_fixed_size 0
		.amdhsa_kernarg_size 56
		.amdhsa_user_sgpr_count 2
		.amdhsa_user_sgpr_dispatch_ptr 0
		.amdhsa_user_sgpr_queue_ptr 0
		.amdhsa_user_sgpr_kernarg_segment_ptr 1
		.amdhsa_user_sgpr_dispatch_id 0
		.amdhsa_user_sgpr_kernarg_preload_length 0
		.amdhsa_user_sgpr_kernarg_preload_offset 0
		.amdhsa_user_sgpr_private_segment_size 0
		.amdhsa_uses_dynamic_stack 0
		.amdhsa_enable_private_segment 0
		.amdhsa_system_sgpr_workgroup_id_x 1
		.amdhsa_system_sgpr_workgroup_id_y 0
		.amdhsa_system_sgpr_workgroup_id_z 0
		.amdhsa_system_sgpr_workgroup_info 0
		.amdhsa_system_vgpr_workitem_id 0
		.amdhsa_next_free_vgpr 256
		.amdhsa_next_free_sgpr 96
		.amdhsa_accum_offset 256
		.amdhsa_reserve_vcc 1
		.amdhsa_float_round_mode_32 0
		.amdhsa_float_round_mode_16_64 0
		.amdhsa_float_denorm_mode_32 3
		.amdhsa_float_denorm_mode_16_64 3
		.amdhsa_dx10_clamp 1
		.amdhsa_ieee_mode 1
		.amdhsa_fp16_overflow 0
		.amdhsa_tg_split 0
		.amdhsa_exception_fp_ieee_invalid_op 0
		.amdhsa_exception_fp_denorm_src 0
		.amdhsa_exception_fp_ieee_div_zero 0
		.amdhsa_exception_fp_ieee_overflow 0
		.amdhsa_exception_fp_ieee_underflow 0
		.amdhsa_exception_fp_ieee_inexact 0
		.amdhsa_exception_int_div_zero 0
	.end_amdhsa_kernel

amdhsa.kernels:
  - .agpr_count:     0
    .args:
      - .actual_access:  read_only
        .address_space:  global
        .offset:         0
        .size:           8
        .value_kind:     global_buffer
      - .actual_access:  read_only
        .address_space:  global
        .offset:         8
        .size:           8
        .value_kind:     global_buffer
      - .actual_access:  read_only
        .address_space:  global
        .offset:         16
        .size:           8
        .value_kind:     global_buffer
      - .actual_access:  write_only
        .address_space:  global
        .offset:         24
        .size:           8
        .value_kind:     global_buffer
      - .actual_access:  write_only
        .address_space:  global
        .offset:         32
        .size:           8
        .value_kind:     global_buffer
      - .actual_access:  write_only
        .address_space:  global
        .offset:         40
        .size:           8
        .value_kind:     global_buffer
      - .actual_access:  write_only
        .address_space:  global
        .offset:         48
        .size:           8
        .value_kind:     global_buffer
      - .actual_access:  write_only
        .address_space:  global
        .offset:         56
        .size:           8
        .value_kind:     global_buffer
      - .actual_access:  write_only
        .address_space:  global
        .offset:         64
        .size:           8
        .value_kind:     global_buffer
      - .actual_access:  write_only
        .address_space:  global
        .offset:         72
        .size:           8
        .value_kind:     global_buffer
      - .actual_access:  write_only
        .address_space:  global
        .offset:         80
        .size:           8
        .value_kind:     global_buffer
    .group_segment_fixed_size: 49152
    .kernarg_segment_align: 8
    .kernarg_segment_size: 88
    .language:       OpenCL C
    .language_version:
      - 2
      - 0
    .max_flat_workgroup_size: 256
    .name:           _Z12quant_kernelPKfS0_PKiPhS3_PjS4_PfS5_S5_Pi
    .private_segment_fixed_size: 0
    .sgpr_count:     31
    .sgpr_spill_count: 0
    .symbol:         _Z12quant_kernelPKfS0_PKiPhS3_PjS4_PfS5_S5_Pi.kd
    .uniform_work_group_size: 1
    .uses_dynamic_stack: false
    .vgpr_count:     163
    .vgpr_spill_count: 0
    .wavefront_size: 64
  - .agpr_count:     0
    .args:
      - .actual_access:  read_only
        .address_space:  global
        .offset:         0
        .size:           8
        .value_kind:     global_buffer
      - .actual_access:  read_only
        .address_space:  global
        .offset:         8
        .size:           8
        .value_kind:     global_buffer
      - .address_space:  global
        .offset:         16
        .size:           8
        .value_kind:     global_buffer
      - .address_space:  global
        .offset:         24
        .size:           8
        .value_kind:     global_buffer
      - .address_space:  global
        .offset:         32
        .size:           8
        .value_kind:     global_buffer
      - .address_space:  global
        .offset:         40
        .size:           8
        .value_kind:     global_buffer
      - .actual_access:  write_only
        .address_space:  global
        .offset:         48
        .size:           8
        .value_kind:     global_buffer
    .group_segment_fixed_size: 126976
    .kernarg_segment_align: 8
    .kernarg_segment_size: 56
    .language:       OpenCL C
    .language_version:
      - 2
      - 0
    .max_flat_workgroup_size: 512
    .name:           _Z15gemm_lse_kernelPKhS0_PKjS2_PfPiP15HIP_vector_typeIfLj2EE
    .private_segment_fixed_size: 0
    .sgpr_count:     48
    .sgpr_spill_count: 0
    .symbol:         _Z15gemm_lse_kernelPKhS0_PKjS2_PfPiP15HIP_vector_typeIfLj2EE.kd
    .uniform_work_group_size: 1
    .uses_dynamic_stack: false
    .vgpr_count:     256
    .vgpr_spill_count: 0
    .wavefront_size: 64
  - .agpr_count:     0
    .args:
      - .actual_access:  read_only
        .address_space:  global
        .offset:         0
        .size:           8
        .value_kind:     global_buffer
      - .actual_access:  read_only
        .address_space:  global
        .offset:         8
        .size:           8
        .value_kind:     global_buffer
      - .actual_access:  read_only
        .address_space:  global
        .offset:         16
        .size:           8
        .value_kind:     global_buffer
      - .actual_access:  read_only
        .address_space:  global
        .offset:         24
        .size:           8
        .value_kind:     global_buffer
      - .actual_access:  read_only
        .address_space:  global
        .offset:         32
        .size:           8
        .value_kind:     global_buffer
      - .actual_access:  read_only
        .address_space:  global
        .offset:         40
        .size:           8
        .value_kind:     global_buffer
      - .address_space:  global
        .offset:         48
        .size:           8
        .value_kind:     global_buffer
    .group_segment_fixed_size: 16
    .kernarg_segment_align: 8
    .kernarg_segment_size: 56
    .language:       OpenCL C
    .language_version:
      - 2
      - 0
    .max_flat_workgroup_size: 256
    .name:           _Z15finalize_kernelPKfPKiPK15HIP_vector_typeIfLj2EES0_S2_S2_Pf
    .private_segment_fixed_size: 0
    .sgpr_count:     33
    .sgpr_spill_count: 0
    .symbol:         _Z15finalize_kernelPKfPKiPK15HIP_vector_typeIfLj2EES0_S2_S2_Pf.kd
    .uniform_work_group_size: 1
    .uses_dynamic_stack: false
    .vgpr_count:     19
    .vgpr_spill_count: 0
    .wavefront_size: 64
